# down GEMM: first K-tile pair's counted waits 16 to 26 (the 10 prefetched epilogue operand loads are also younger than the loads they retire) + down epilogue wait fix + final RMSNorm rewrite
# baseline (speedup 1.0000x reference)
.LBB0_1623:
	s_ashr_i32 s41, s40, 31
	s_lshl_b64 s[8:9], s[40:41], 18
	s_add_u32 s44, s33, s8
	ds_read_b128 v[10:13], v162
	ds_read_b128 v[14:17], v162 offset:1024
	ds_read_b128 v[26:29], v162 offset:2048
	ds_read_b128 v[30:33], v162 offset:3072
	ds_read_b128 v[172:175], v163
	ds_read_b128 v[176:179], v163 offset:1024
	ds_read_b128 v[180:183], v163 offset:2048
	ds_read_b128 v[184:187], v163 offset:3072
	s_addc_u32 s45, s37, s9
	s_and_b64 s[8:9], s[6:7], exec
	s_cselect_b32 s75, s45, s69
	s_cselect_b32 s74, s44, s68
	s_ashr_i32 s43, s42, 31
	s_ashr_i32 s39, s38, 31
	s_lshl_b64 s[8:9], s[42:43], 20
	s_lshl_b64 s[46:47], s[38:39], 18
	s_add_u32 s8, s54, s8
	s_addc_u32 s9, s55, s9
	s_add_u32 s46, s8, s46
	s_addc_u32 s47, s9, s47
	s_and_b64 s[8:9], s[6:7], exec
	s_cselect_b32 s9, s47, s73
	s_cselect_b32 s8, s46, s72
	ds_read_b128 v[18:21], v161
	ds_read_b128 v[22:25], v161 offset:1024
	ds_read_b128 v[34:37], v161 offset:2048
	ds_read_b128 v[38:41], v161 offset:3072
	ds_read_b128 v[42:45], v161 offset:4096
	ds_read_b128 v[46:49], v161 offset:5120
	ds_read_b128 v[50:53], v161 offset:6144
	ds_read_b128 v[54:57], v161 offset:7168
	s_waitcnt vmcnt(26)
	s_waitcnt lgkmcnt(0)
	s_barrier
	s_setprio 1
	s_waitcnt lgkmcnt(0)
	v_mfma_f32_16x16x128_f8f6f4 v[134:137], v[10:17], v[18:25], 0
	v_mfma_f32_16x16x128_f8f6f4 v[130:133], v[26:33], v[18:25], 0
	v_mfma_f32_16x16x128_f8f6f4 v[118:121], v[10:17], v[34:41], 0
	v_mfma_f32_16x16x128_f8f6f4 v[114:117], v[26:33], v[34:41], 0
	v_mfma_f32_16x16x128_f8f6f4 v[102:105], v[10:17], v[42:49], 0
	v_mfma_f32_16x16x128_f8f6f4 v[98:101], v[26:33], v[42:49], 0
	v_mfma_f32_16x16x128_f8f6f4 v[78:81], v[10:17], v[50:57], 0
	v_mfma_f32_16x16x128_f8f6f4 v[74:77], v[26:33], v[50:57], 0
	s_setprio 0
	s_setprio 1
	v_mfma_f32_16x16x128_f8f6f4 v[126:129], v[172:179], v[18:25], 0
	v_mfma_f32_16x16x128_f8f6f4 v[122:125], v[180:187], v[18:25], 0
	v_mfma_f32_16x16x128_f8f6f4 v[110:113], v[172:179], v[34:41], 0
	v_mfma_f32_16x16x128_f8f6f4 v[106:109], v[180:187], v[34:41], 0
	v_mfma_f32_16x16x128_f8f6f4 v[94:97], v[172:179], v[42:49], 0
	v_mfma_f32_16x16x128_f8f6f4 v[90:93], v[180:187], v[42:49], 0
	v_mfma_f32_16x16x128_f8f6f4 v[62:65], v[172:179], v[50:57], 0
	v_mfma_f32_16x16x128_f8f6f4 v[58:61], v[180:187], v[50:57], 0
	s_setprio 0
	s_barrier
	s_add_i32 s80, s66, s58
	v_lshl_add_u64 v[150:151], s[72:73], 0, v[140:141]
	s_add_i32 s76, s80, 0x2000
	v_lshl_add_u64 v[18:19], v[150:151], 0, s[22:23]
	s_mov_b32 m0, s80
	v_lshl_add_u64 v[152:153], s[72:73], 0, v[144:145]
	s_add_u32 s78, s72, 0x8100
	ds_read_b128 v[42:45], v161 offset:16384
	ds_read_b128 v[46:49], v161 offset:17408
	ds_read_b128 v[188:191], v161 offset:18432
	ds_read_b128 v[192:195], v161 offset:19456
	ds_read_b128 v[204:207], v161 offset:20480
	ds_read_b128 v[208:211], v161 offset:21504
	ds_read_b128 v[212:215], v161 offset:22528
	ds_read_b128 v[216:219], v161 offset:23552
	global_load_lds_dwordx4 v[18:19], off
	v_lshl_add_u64 v[18:19], v[152:153], 0, s[22:23]
	s_mov_b32 m0, s76
	s_addc_u32 s79, s73, 0
	s_add_i32 s77, s67, s58
	global_load_lds_dwordx4 v[18:19], off
	v_lshl_add_u64 v[18:19], s[78:79], 0, v[140:141]
	s_mov_b32 m0, s77
	v_lshl_add_u64 v[154:155], s[68:69], 0, v[138:139]
	global_load_lds_dwordx4 v[18:19], off
	v_lshl_add_u64 v[18:19], s[78:79], 0, v[144:145]
	s_add_i32 s78, s77, 0x2000
	s_mov_b32 m0, s78
	v_lshl_add_u64 v[156:157], s[68:69], 0, v[142:143]
	global_load_lds_dwordx4 v[18:19], off
	v_lshl_add_u64 v[18:19], v[154:155], 0, s[22:23]
	s_mov_b32 m0, s49
	s_nop 0
	global_load_lds_dwordx4 v[18:19], off
	v_lshl_add_u64 v[18:19], v[156:157], 0, s[22:23]
	s_mov_b32 m0, s51
	s_nop 0
	global_load_lds_dwordx4 v[18:19], off
	s_waitcnt vmcnt(26)
	s_waitcnt lgkmcnt(0)
	s_barrier
	s_setprio 1
	s_waitcnt lgkmcnt(0)
	v_mfma_f32_16x16x128_f8f6f4 v[86:89], v[10:17], v[42:49], 0
	v_mfma_f32_16x16x128_f8f6f4 v[82:85], v[26:33], v[42:49], 0
	v_mfma_f32_16x16x128_f8f6f4 v[54:57], v[10:17], v[188:195], 0
	v_mfma_f32_16x16x128_f8f6f4 v[50:53], v[26:33], v[188:195], 0
	v_mfma_f32_16x16x128_f8f6f4 v[38:41], v[10:17], v[204:211], 0
	v_mfma_f32_16x16x128_f8f6f4 v[34:37], v[26:33], v[204:211], 0
	v_mfma_f32_16x16x128_f8f6f4 v[22:25], v[10:17], v[212:219], 0
	v_mfma_f32_16x16x128_f8f6f4 v[18:21], v[26:33], v[212:219], 0
	s_setprio 0
	s_setprio 1
	v_mfma_f32_16x16x128_f8f6f4 v[70:73], v[172:179], v[42:49], 0
	v_mfma_f32_16x16x128_f8f6f4 v[66:69], v[180:187], v[42:49], 0
	v_mfma_f32_16x16x128_f8f6f4 v[46:49], v[172:179], v[188:195], 0
	v_mfma_f32_16x16x128_f8f6f4 v[42:45], v[180:187], v[188:195], 0
	v_mfma_f32_16x16x128_f8f6f4 v[30:33], v[172:179], v[204:211], 0
	v_mfma_f32_16x16x128_f8f6f4 v[26:29], v[180:187], v[204:211], 0
	v_mfma_f32_16x16x128_f8f6f4 v[14:17], v[172:179], v[212:219], 0
	v_mfma_f32_16x16x128_f8f6f4 v[10:13], v[180:187], v[212:219], 0
	s_setprio 0
	s_barrier
	s_add_i32 s79, 0, 0x18000
	s_add_i32 s41, 0, 0x1c000
	v_add_u32_e32 v158, s79, v160
	v_add_u32_e32 v159, s41, v160
	ds_read_b128 v[172:175], v158
	ds_read_b128 v[176:179], v158 offset:1024
	ds_read_b128 v[180:183], v158 offset:2048
	ds_read_b128 v[184:187], v158 offset:3072
	ds_read_b128 v[188:191], v159
	ds_read_b128 v[192:195], v159 offset:1024
	ds_read_b128 v[204:207], v159 offset:2048
	ds_read_b128 v[208:211], v159 offset:3072
	s_add_u32 s82, s68, 0x20100
	s_addc_u32 s83, s69, 0
	s_mov_b32 m0, s59
	v_lshl_add_u64 v[196:197], s[82:83], 0, v[138:139]
	ds_read_b128 v[212:215], v161 offset:32768
	ds_read_b128 v[216:219], v161 offset:33792
	ds_read_b128 v[220:223], v161 offset:34816
	ds_read_b128 v[224:227], v161 offset:35840
	ds_read_b128 v[228:231], v161 offset:36864
	ds_read_b128 v[232:235], v161 offset:37888
	ds_read_b128 v[236:239], v161 offset:38912
	ds_read_b128 v[240:243], v161 offset:39936
	global_load_lds_dwordx4 v[196:197], off
	v_lshl_add_u64 v[196:197], s[82:83], 0, v[142:143]
	s_mov_b32 m0, s60
	s_nop 0
	global_load_lds_dwordx4 v[196:197], off
	s_waitcnt vmcnt(26)
	s_waitcnt lgkmcnt(0)
	s_barrier
	s_setprio 1
	s_waitcnt lgkmcnt(0)
	v_mfma_f32_16x16x128_f8f6f4 v[134:137], v[172:179], v[212:219], v[134:137]
	v_mfma_f32_16x16x128_f8f6f4 v[130:133], v[180:187], v[212:219], v[130:133]
	v_mfma_f32_16x16x128_f8f6f4 v[118:121], v[172:179], v[220:227], v[118:121]
	v_mfma_f32_16x16x128_f8f6f4 v[114:117], v[180:187], v[220:227], v[114:117]
	v_mfma_f32_16x16x128_f8f6f4 v[102:105], v[172:179], v[228:235], v[102:105]
	v_mfma_f32_16x16x128_f8f6f4 v[98:101], v[180:187], v[228:235], v[98:101]
	v_mfma_f32_16x16x128_f8f6f4 v[78:81], v[172:179], v[236:243], v[78:81]
	v_mfma_f32_16x16x128_f8f6f4 v[74:77], v[180:187], v[236:243], v[74:77]
	s_setprio 0
	s_setprio 1
	v_mfma_f32_16x16x128_f8f6f4 v[126:129], v[188:195], v[212:219], v[126:129]
	v_mfma_f32_16x16x128_f8f6f4 v[122:125], v[204:211], v[212:219], v[122:125]
	v_mfma_f32_16x16x128_f8f6f4 v[110:113], v[188:195], v[220:227], v[110:113]
	v_mfma_f32_16x16x128_f8f6f4 v[106:109], v[204:211], v[220:227], v[106:109]
	v_mfma_f32_16x16x128_f8f6f4 v[94:97], v[188:195], v[228:235], v[94:97]
	v_mfma_f32_16x16x128_f8f6f4 v[90:93], v[204:211], v[228:235], v[90:93]
	v_mfma_f32_16x16x128_f8f6f4 v[62:65], v[188:195], v[236:243], v[62:65]
	v_mfma_f32_16x16x128_f8f6f4 v[58:61], v[204:211], v[236:243], v[58:61]
	s_setprio 0
	s_barrier
	s_add_i32 s79, s79, s58
	s_add_i32 s39, s79, 0x2000
	v_lshl_add_u64 v[196:197], v[150:151], 0, s[24:25]
	s_mov_b32 m0, s79
	s_add_u32 s82, s72, 0x8180
	ds_read_b128 v[212:215], v161 offset:49152
	ds_read_b128 v[216:219], v161 offset:50176
	ds_read_b128 v[220:223], v161 offset:51200
	ds_read_b128 v[224:227], v161 offset:52224
	ds_read_b128 v[228:231], v161 offset:53248
	ds_read_b128 v[232:235], v161 offset:54272
	ds_read_b128 v[236:239], v161 offset:55296
	ds_read_b128 v[240:243], v161 offset:56320
	global_load_lds_dwordx4 v[196:197], off
	v_lshl_add_u64 v[196:197], v[152:153], 0, s[24:25]
	s_mov_b32 m0, s39
	s_addc_u32 s83, s73, 0
	s_add_i32 s41, s41, s58
	global_load_lds_dwordx4 v[196:197], off
	v_lshl_add_u64 v[196:197], s[82:83], 0, v[140:141]
	s_mov_b32 m0, s41
	s_add_i32 s71, s41, 0x2000
	global_load_lds_dwordx4 v[196:197], off
	v_lshl_add_u64 v[196:197], s[82:83], 0, v[144:145]
	s_mov_b32 m0, s71
	s_nop 0
	global_load_lds_dwordx4 v[196:197], off
	v_lshl_add_u64 v[196:197], v[154:155], 0, s[24:25]
	s_mov_b32 m0, s61
	s_nop 0
	global_load_lds_dwordx4 v[196:197], off
	v_lshl_add_u64 v[196:197], v[156:157], 0, s[24:25]
	s_mov_b32 m0, s62
	s_nop 0
	global_load_lds_dwordx4 v[196:197], off
	s_waitcnt vmcnt(8)
	s_waitcnt lgkmcnt(0)
	s_barrier
	s_setprio 1
	s_waitcnt lgkmcnt(0)
	v_mfma_f32_16x16x128_f8f6f4 v[86:89], v[172:179], v[212:219], v[86:89]
	v_mfma_f32_16x16x128_f8f6f4 v[82:85], v[180:187], v[212:219], v[82:85]
	v_mfma_f32_16x16x128_f8f6f4 v[54:57], v[172:179], v[220:227], v[54:57]
	v_mfma_f32_16x16x128_f8f6f4 v[50:53], v[180:187], v[220:227], v[50:53]
	v_mfma_f32_16x16x128_f8f6f4 v[38:41], v[172:179], v[228:235], v[38:41]
	v_mfma_f32_16x16x128_f8f6f4 v[34:37], v[180:187], v[228:235], v[34:37]
	v_mfma_f32_16x16x128_f8f6f4 v[22:25], v[172:179], v[236:243], v[22:25]
	v_mfma_f32_16x16x128_f8f6f4 v[18:21], v[180:187], v[236:243], v[18:21]
	s_setprio 0
	s_setprio 1
	v_mfma_f32_16x16x128_f8f6f4 v[70:73], v[188:195], v[212:219], v[70:73]
	v_mfma_f32_16x16x128_f8f6f4 v[66:69], v[204:211], v[212:219], v[66:69]
	v_mfma_f32_16x16x128_f8f6f4 v[46:49], v[188:195], v[220:227], v[46:49]
	v_mfma_f32_16x16x128_f8f6f4 v[42:45], v[204:211], v[220:227], v[42:45]
	v_mfma_f32_16x16x128_f8f6f4 v[30:33], v[188:195], v[228:235], v[30:33]
	v_mfma_f32_16x16x128_f8f6f4 v[26:29], v[204:211], v[228:235], v[26:29]
	v_mfma_f32_16x16x128_f8f6f4 v[14:17], v[188:195], v[236:243], v[14:17]
	v_mfma_f32_16x16x128_f8f6f4 v[10:13], v[204:211], v[236:243], v[10:13]
	s_setprio 0
	s_barrier
	ds_read_b128 v[172:175], v162
	ds_read_b128 v[176:179], v162 offset:1024
	ds_read_b128 v[180:183], v162 offset:2048
	ds_read_b128 v[184:187], v162 offset:3072
	ds_read_b128 v[188:191], v163
	ds_read_b128 v[192:195], v163 offset:1024
	ds_read_b128 v[204:207], v163 offset:2048
	ds_read_b128 v[208:211], v163 offset:3072
	s_add_u32 s82, s68, 0x20180
	s_addc_u32 s83, s69, 0
	s_mov_b32 m0, s63
	v_lshl_add_u64 v[196:197], s[82:83], 0, v[138:139]
	ds_read_b128 v[212:215], v161
	ds_read_b128 v[216:219], v161 offset:1024
	ds_read_b128 v[220:223], v161 offset:2048
	ds_read_b128 v[224:227], v161 offset:3072
	ds_read_b128 v[228:231], v161 offset:4096
	ds_read_b128 v[232:235], v161 offset:5120
	ds_read_b128 v[236:239], v161 offset:6144
	ds_read_b128 v[240:243], v161 offset:7168
	global_load_lds_dwordx4 v[196:197], off
	v_lshl_add_u64 v[196:197], s[82:83], 0, v[142:143]
	s_mov_b32 m0, s64
	s_nop 0
	global_load_lds_dwordx4 v[196:197], off
	s_waitcnt vmcnt(8)
	s_waitcnt lgkmcnt(0)
	s_barrier
	s_setprio 1
	s_waitcnt lgkmcnt(0)
	v_mfma_f32_16x16x128_f8f6f4 v[134:137], v[172:179], v[212:219], v[134:137]
	v_mfma_f32_16x16x128_f8f6f4 v[130:133], v[180:187], v[212:219], v[130:133]
	v_mfma_f32_16x16x128_f8f6f4 v[118:121], v[172:179], v[220:227], v[118:121]
	v_mfma_f32_16x16x128_f8f6f4 v[114:117], v[180:187], v[220:227], v[114:117]
	v_mfma_f32_16x16x128_f8f6f4 v[102:105], v[172:179], v[228:235], v[102:105]
	v_mfma_f32_16x16x128_f8f6f4 v[98:101], v[180:187], v[228:235], v[98:101]
	v_mfma_f32_16x16x128_f8f6f4 v[78:81], v[172:179], v[236:243], v[78:81]
	v_mfma_f32_16x16x128_f8f6f4 v[74:77], v[180:187], v[236:243], v[74:77]
	s_setprio 0
	s_setprio 1
	v_mfma_f32_16x16x128_f8f6f4 v[126:129], v[188:195], v[212:219], v[126:129]
	v_mfma_f32_16x16x128_f8f6f4 v[122:125], v[204:211], v[212:219], v[122:125]
	v_mfma_f32_16x16x128_f8f6f4 v[110:113], v[188:195], v[220:227], v[110:113]
	v_mfma_f32_16x16x128_f8f6f4 v[106:109], v[204:211], v[220:227], v[106:109]
	v_mfma_f32_16x16x128_f8f6f4 v[94:97], v[188:195], v[228:235], v[94:97]
	v_mfma_f32_16x16x128_f8f6f4 v[90:93], v[204:211], v[228:235], v[90:93]
	v_mfma_f32_16x16x128_f8f6f4 v[62:65], v[188:195], v[236:243], v[62:65]
	v_mfma_f32_16x16x128_f8f6f4 v[58:61], v[204:211], v[236:243], v[58:61]
	s_setprio 0
	s_barrier
	s_mov_b32 m0, s80
	v_lshl_add_u64 v[196:197], v[150:151], 0, s[26:27]
	s_add_u32 s82, s72, 0x8200
	ds_read_b128 v[212:215], v161 offset:16384
	ds_read_b128 v[216:219], v161 offset:17408
	ds_read_b128 v[220:223], v161 offset:18432
	ds_read_b128 v[224:227], v161 offset:19456
	ds_read_b128 v[228:231], v161 offset:20480
	ds_read_b128 v[232:235], v161 offset:21504
	ds_read_b128 v[236:239], v161 offset:22528
	ds_read_b128 v[240:243], v161 offset:23552
	global_load_lds_dwordx4 v[196:197], off
	v_lshl_add_u64 v[196:197], v[152:153], 0, s[26:27]
	s_mov_b32 m0, s76
	s_addc_u32 s83, s73, 0
	global_load_lds_dwordx4 v[196:197], off
	v_lshl_add_u64 v[196:197], s[82:83], 0, v[140:141]
	s_mov_b32 m0, s77
	s_nop 0
	global_load_lds_dwordx4 v[196:197], off
	v_lshl_add_u64 v[196:197], s[82:83], 0, v[144:145]
	s_mov_b32 m0, s78
	s_nop 0
	global_load_lds_dwordx4 v[196:197], off
	v_lshl_add_u64 v[196:197], v[154:155], 0, s[26:27]
	s_mov_b32 m0, s49
	s_nop 0
	global_load_lds_dwordx4 v[196:197], off
	v_lshl_add_u64 v[196:197], v[156:157], 0, s[26:27]
	s_mov_b32 m0, s51
	s_nop 0
	global_load_lds_dwordx4 v[196:197], off
	s_waitcnt vmcnt(8)
	s_waitcnt lgkmcnt(0)
	s_barrier
	s_setprio 1
	s_waitcnt lgkmcnt(0)
	v_mfma_f32_16x16x128_f8f6f4 v[86:89], v[172:179], v[212:219], v[86:89]
	v_mfma_f32_16x16x128_f8f6f4 v[82:85], v[180:187], v[212:219], v[82:85]
	v_mfma_f32_16x16x128_f8f6f4 v[54:57], v[172:179], v[220:227], v[54:57]
	v_mfma_f32_16x16x128_f8f6f4 v[50:53], v[180:187], v[220:227], v[50:53]
	v_mfma_f32_16x16x128_f8f6f4 v[38:41], v[172:179], v[228:235], v[38:41]
	v_mfma_f32_16x16x128_f8f6f4 v[34:37], v[180:187], v[228:235], v[34:37]
	v_mfma_f32_16x16x128_f8f6f4 v[22:25], v[172:179], v[236:243], v[22:25]
	v_mfma_f32_16x16x128_f8f6f4 v[18:21], v[180:187], v[236:243], v[18:21]
	s_setprio 0
	s_setprio 1
	v_mfma_f32_16x16x128_f8f6f4 v[70:73], v[188:195], v[212:219], v[70:73]
	v_mfma_f32_16x16x128_f8f6f4 v[66:69], v[204:211], v[212:219], v[66:69]
	v_mfma_f32_16x16x128_f8f6f4 v[46:49], v[188:195], v[220:227], v[46:49]
	v_mfma_f32_16x16x128_f8f6f4 v[42:45], v[204:211], v[220:227], v[42:45]
	v_mfma_f32_16x16x128_f8f6f4 v[30:33], v[188:195], v[228:235], v[30:33]
	v_mfma_f32_16x16x128_f8f6f4 v[26:29], v[204:211], v[228:235], v[26:29]
	v_mfma_f32_16x16x128_f8f6f4 v[14:17], v[188:195], v[236:243], v[14:17]
	v_mfma_f32_16x16x128_f8f6f4 v[10:13], v[204:211], v[236:243], v[10:13]
	s_setprio 0
	s_barrier
	ds_read_b128 v[172:175], v158
	ds_read_b128 v[176:179], v158 offset:1024
	ds_read_b128 v[180:183], v158 offset:2048
	ds_read_b128 v[184:187], v158 offset:3072
	ds_read_b128 v[188:191], v159
	ds_read_b128 v[192:195], v159 offset:1024
	ds_read_b128 v[204:207], v159 offset:2048
	ds_read_b128 v[208:211], v159 offset:3072
	s_add_u32 s82, s68, 0x20200
	s_addc_u32 s83, s69, 0
	s_mov_b32 m0, s59
	v_lshl_add_u64 v[196:197], s[82:83], 0, v[138:139]
	ds_read_b128 v[212:215], v161 offset:32768
	ds_read_b128 v[216:219], v161 offset:33792
	ds_read_b128 v[220:223], v161 offset:34816
	ds_read_b128 v[224:227], v161 offset:35840
	ds_read_b128 v[228:231], v161 offset:36864
	ds_read_b128 v[232:235], v161 offset:37888
	ds_read_b128 v[236:239], v161 offset:38912
	ds_read_b128 v[240:243], v161 offset:39936
	global_load_lds_dwordx4 v[196:197], off
	v_lshl_add_u64 v[196:197], s[82:83], 0, v[142:143]
	s_mov_b32 m0, s60
	s_nop 0
	global_load_lds_dwordx4 v[196:197], off
	s_waitcnt vmcnt(8)
	s_waitcnt lgkmcnt(0)
	s_barrier
	s_setprio 1
	s_waitcnt lgkmcnt(0)
	v_mfma_f32_16x16x128_f8f6f4 v[134:137], v[172:179], v[212:219], v[134:137]
	v_mfma_f32_16x16x128_f8f6f4 v[130:133], v[180:187], v[212:219], v[130:133]
	v_mfma_f32_16x16x128_f8f6f4 v[118:121], v[172:179], v[220:227], v[118:121]
	v_mfma_f32_16x16x128_f8f6f4 v[114:117], v[180:187], v[220:227], v[114:117]
	v_mfma_f32_16x16x128_f8f6f4 v[102:105], v[172:179], v[228:235], v[102:105]
	v_mfma_f32_16x16x128_f8f6f4 v[98:101], v[180:187], v[228:235], v[98:101]
	v_mfma_f32_16x16x128_f8f6f4 v[78:81], v[172:179], v[236:243], v[78:81]
	v_mfma_f32_16x16x128_f8f6f4 v[74:77], v[180:187], v[236:243], v[74:77]
	s_setprio 0
	s_setprio 1
	v_mfma_f32_16x16x128_f8f6f4 v[126:129], v[188:195], v[212:219], v[126:129]
	v_mfma_f32_16x16x128_f8f6f4 v[122:125], v[204:211], v[212:219], v[122:125]
	v_mfma_f32_16x16x128_f8f6f4 v[110:113], v[188:195], v[220:227], v[110:113]
	v_mfma_f32_16x16x128_f8f6f4 v[106:109], v[204:211], v[220:227], v[106:109]
	v_mfma_f32_16x16x128_f8f6f4 v[94:97], v[188:195], v[228:235], v[94:97]
	v_mfma_f32_16x16x128_f8f6f4 v[90:93], v[204:211], v[228:235], v[90:93]
	v_mfma_f32_16x16x128_f8f6f4 v[62:65], v[188:195], v[236:243], v[62:65]
	v_mfma_f32_16x16x128_f8f6f4 v[58:61], v[204:211], v[236:243], v[58:61]
	s_setprio 0
	s_barrier
	s_mov_b32 m0, s79
	v_lshl_add_u64 v[196:197], v[150:151], 0, s[28:29]
	s_add_u32 s82, s72, 0x8280
	ds_read_b128 v[212:215], v161 offset:49152
	ds_read_b128 v[216:219], v161 offset:50176
	ds_read_b128 v[220:223], v161 offset:51200
	ds_read_b128 v[224:227], v161 offset:52224
	ds_read_b128 v[228:231], v161 offset:53248
	ds_read_b128 v[232:235], v161 offset:54272
	ds_read_b128 v[236:239], v161 offset:55296
	ds_read_b128 v[240:243], v161 offset:56320
	global_load_lds_dwordx4 v[196:197], off
	v_lshl_add_u64 v[196:197], v[152:153], 0, s[28:29]
	s_mov_b32 m0, s39
	s_addc_u32 s83, s73, 0
	global_load_lds_dwordx4 v[196:197], off
	v_lshl_add_u64 v[196:197], s[82:83], 0, v[140:141]
	s_mov_b32 m0, s41
	s_nop 0
	global_load_lds_dwordx4 v[196:197], off
	v_lshl_add_u64 v[196:197], s[82:83], 0, v[144:145]
	s_mov_b32 m0, s71
	s_nop 0
	global_load_lds_dwordx4 v[196:197], off
	v_lshl_add_u64 v[196:197], v[154:155], 0, s[28:29]
	s_mov_b32 m0, s61
	s_nop 0
	global_load_lds_dwordx4 v[196:197], off
	v_lshl_add_u64 v[196:197], v[156:157], 0, s[28:29]
	s_mov_b32 m0, s62
	s_nop 0
	global_load_lds_dwordx4 v[196:197], off
	s_waitcnt vmcnt(8)
	s_waitcnt lgkmcnt(0)
	s_barrier
	s_setprio 1
	s_waitcnt lgkmcnt(0)
	v_mfma_f32_16x16x128_f8f6f4 v[86:89], v[172:179], v[212:219], v[86:89]
	v_mfma_f32_16x16x128_f8f6f4 v[82:85], v[180:187], v[212:219], v[82:85]
	v_mfma_f32_16x16x128_f8f6f4 v[54:57], v[172:179], v[220:227], v[54:57]
	v_mfma_f32_16x16x128_f8f6f4 v[50:53], v[180:187], v[220:227], v[50:53]
	v_mfma_f32_16x16x128_f8f6f4 v[38:41], v[172:179], v[228:235], v[38:41]
	v_mfma_f32_16x16x128_f8f6f4 v[34:37], v[180:187], v[228:235], v[34:37]
	v_mfma_f32_16x16x128_f8f6f4 v[22:25], v[172:179], v[236:243], v[22:25]
	v_mfma_f32_16x16x128_f8f6f4 v[18:21], v[180:187], v[236:243], v[18:21]
	s_setprio 0
	s_setprio 1
	v_mfma_f32_16x16x128_f8f6f4 v[70:73], v[188:195], v[212:219], v[70:73]
	v_mfma_f32_16x16x128_f8f6f4 v[66:69], v[204:211], v[212:219], v[66:69]
	v_mfma_f32_16x16x128_f8f6f4 v[46:49], v[188:195], v[220:227], v[46:49]
	v_mfma_f32_16x16x128_f8f6f4 v[42:45], v[204:211], v[220:227], v[42:45]
	v_mfma_f32_16x16x128_f8f6f4 v[30:33], v[188:195], v[228:235], v[30:33]
	v_mfma_f32_16x16x128_f8f6f4 v[26:29], v[204:211], v[228:235], v[26:29]
	v_mfma_f32_16x16x128_f8f6f4 v[14:17], v[188:195], v[236:243], v[14:17]
	v_mfma_f32_16x16x128_f8f6f4 v[10:13], v[204:211], v[236:243], v[10:13]
	s_setprio 0
	s_barrier
	ds_read_b128 v[172:175], v162
	ds_read_b128 v[176:179], v162 offset:1024
	ds_read_b128 v[180:183], v162 offset:2048
	ds_read_b128 v[184:187], v162 offset:3072
	ds_read_b128 v[188:191], v163
	ds_read_b128 v[192:195], v163 offset:1024
	ds_read_b128 v[204:207], v163 offset:2048
	ds_read_b128 v[208:211], v163 offset:3072
	s_add_u32 s82, s68, 0x20280
	s_addc_u32 s83, s69, 0
	s_mov_b32 m0, s63
	v_lshl_add_u64 v[196:197], s[82:83], 0, v[138:139]
	ds_read_b128 v[212:215], v161
	ds_read_b128 v[216:219], v161 offset:1024
	ds_read_b128 v[220:223], v161 offset:2048
	ds_read_b128 v[224:227], v161 offset:3072
	ds_read_b128 v[228:231], v161 offset:4096
	ds_read_b128 v[232:235], v161 offset:5120
	ds_read_b128 v[236:239], v161 offset:6144
	ds_read_b128 v[240:243], v161 offset:7168
	global_load_lds_dwordx4 v[196:197], off
	v_lshl_add_u64 v[196:197], s[82:83], 0, v[142:143]
	s_mov_b32 m0, s64
	s_nop 0
	global_load_lds_dwordx4 v[196:197], off
	s_waitcnt vmcnt(8)
	s_waitcnt lgkmcnt(0)
	s_barrier
	s_setprio 1
	s_waitcnt lgkmcnt(0)
	v_mfma_f32_16x16x128_f8f6f4 v[134:137], v[172:179], v[212:219], v[134:137]
	v_mfma_f32_16x16x128_f8f6f4 v[130:133], v[180:187], v[212:219], v[130:133]
	v_mfma_f32_16x16x128_f8f6f4 v[118:121], v[172:179], v[220:227], v[118:121]
	v_mfma_f32_16x16x128_f8f6f4 v[114:117], v[180:187], v[220:227], v[114:117]
	v_mfma_f32_16x16x128_f8f6f4 v[102:105], v[172:179], v[228:235], v[102:105]
	v_mfma_f32_16x16x128_f8f6f4 v[98:101], v[180:187], v[228:235], v[98:101]
	v_mfma_f32_16x16x128_f8f6f4 v[78:81], v[172:179], v[236:243], v[78:81]
	v_mfma_f32_16x16x128_f8f6f4 v[74:77], v[180:187], v[236:243], v[74:77]
	s_setprio 0
	s_setprio 1
	v_mfma_f32_16x16x128_f8f6f4 v[126:129], v[188:195], v[212:219], v[126:129]
	v_mfma_f32_16x16x128_f8f6f4 v[122:125], v[204:211], v[212:219], v[122:125]
	v_mfma_f32_16x16x128_f8f6f4 v[110:113], v[188:195], v[220:227], v[110:113]
	v_mfma_f32_16x16x128_f8f6f4 v[106:109], v[204:211], v[220:227], v[106:109]
	v_mfma_f32_16x16x128_f8f6f4 v[94:97], v[188:195], v[228:235], v[94:97]
	v_mfma_f32_16x16x128_f8f6f4 v[90:93], v[204:211], v[228:235], v[90:93]
	v_mfma_f32_16x16x128_f8f6f4 v[62:65], v[188:195], v[236:243], v[62:65]
	v_mfma_f32_16x16x128_f8f6f4 v[58:61], v[204:211], v[236:243], v[58:61]
	s_setprio 0
	s_barrier
	s_mov_b32 m0, s80
	v_lshl_add_u64 v[196:197], v[150:151], 0, s[30:31]
	s_add_u32 s82, s72, 0x8300
	ds_read_b128 v[212:215], v161 offset:16384
	ds_read_b128 v[216:219], v161 offset:17408
	ds_read_b128 v[220:223], v161 offset:18432
	ds_read_b128 v[224:227], v161 offset:19456
	ds_read_b128 v[228:231], v161 offset:20480
	ds_read_b128 v[232:235], v161 offset:21504
	ds_read_b128 v[236:239], v161 offset:22528
	ds_read_b128 v[240:243], v161 offset:23552
	global_load_lds_dwordx4 v[196:197], off
	v_lshl_add_u64 v[196:197], v[152:153], 0, s[30:31]
	s_mov_b32 m0, s76
	s_addc_u32 s83, s73, 0
	global_load_lds_dwordx4 v[196:197], off
	v_lshl_add_u64 v[196:197], s[82:83], 0, v[140:141]
	s_mov_b32 m0, s77
	s_nop 0
	global_load_lds_dwordx4 v[196:197], off
	v_lshl_add_u64 v[196:197], s[82:83], 0, v[144:145]
	s_mov_b32 m0, s78
	s_nop 0
	global_load_lds_dwordx4 v[196:197], off
	v_lshl_add_u64 v[196:197], v[154:155], 0, s[30:31]
	s_mov_b32 m0, s49
	s_nop 0
	global_load_lds_dwordx4 v[196:197], off
	v_lshl_add_u64 v[196:197], v[156:157], 0, s[30:31]
	s_mov_b32 m0, s51
	s_nop 0
	global_load_lds_dwordx4 v[196:197], off
	s_waitcnt vmcnt(8)
	s_waitcnt lgkmcnt(0)
	s_barrier
	s_setprio 1
	s_waitcnt lgkmcnt(0)
	v_mfma_f32_16x16x128_f8f6f4 v[86:89], v[172:179], v[212:219], v[86:89]
	v_mfma_f32_16x16x128_f8f6f4 v[82:85], v[180:187], v[212:219], v[82:85]
	v_mfma_f32_16x16x128_f8f6f4 v[54:57], v[172:179], v[220:227], v[54:57]
	v_mfma_f32_16x16x128_f8f6f4 v[50:53], v[180:187], v[220:227], v[50:53]
	v_mfma_f32_16x16x128_f8f6f4 v[38:41], v[172:179], v[228:235], v[38:41]
	v_mfma_f32_16x16x128_f8f6f4 v[34:37], v[180:187], v[228:235], v[34:37]
	v_mfma_f32_16x16x128_f8f6f4 v[22:25], v[172:179], v[236:243], v[22:25]
	v_mfma_f32_16x16x128_f8f6f4 v[18:21], v[180:187], v[236:243], v[18:21]
	s_setprio 0
	s_setprio 1
	v_mfma_f32_16x16x128_f8f6f4 v[70:73], v[188:195], v[212:219], v[70:73]
	v_mfma_f32_16x16x128_f8f6f4 v[66:69], v[204:211], v[212:219], v[66:69]
	v_mfma_f32_16x16x128_f8f6f4 v[46:49], v[188:195], v[220:227], v[46:49]
	v_mfma_f32_16x16x128_f8f6f4 v[42:45], v[204:211], v[220:227], v[42:45]
	v_mfma_f32_16x16x128_f8f6f4 v[30:33], v[188:195], v[228:235], v[30:33]
	v_mfma_f32_16x16x128_f8f6f4 v[26:29], v[204:211], v[228:235], v[26:29]
	v_mfma_f32_16x16x128_f8f6f4 v[14:17], v[188:195], v[236:243], v[14:17]
	v_mfma_f32_16x16x128_f8f6f4 v[10:13], v[204:211], v[236:243], v[10:13]
	s_setprio 0
	s_barrier
	ds_read_b128 v[172:175], v158
	ds_read_b128 v[176:179], v158 offset:1024
	ds_read_b128 v[180:183], v158 offset:2048
	ds_read_b128 v[184:187], v158 offset:3072
	ds_read_b128 v[188:191], v159
	ds_read_b128 v[192:195], v159 offset:1024
	ds_read_b128 v[204:207], v159 offset:2048
	ds_read_b128 v[208:211], v159 offset:3072
	s_add_u32 s82, s68, 0x20300
	s_addc_u32 s83, s69, 0
	s_mov_b32 m0, s59
	v_lshl_add_u64 v[196:197], s[82:83], 0, v[138:139]
	ds_read_b128 v[212:215], v161 offset:32768
	ds_read_b128 v[216:219], v161 offset:33792
	ds_read_b128 v[220:223], v161 offset:34816
	ds_read_b128 v[224:227], v161 offset:35840
	ds_read_b128 v[228:231], v161 offset:36864
	ds_read_b128 v[232:235], v161 offset:37888
	ds_read_b128 v[236:239], v161 offset:38912
	ds_read_b128 v[240:243], v161 offset:39936
	global_load_lds_dwordx4 v[196:197], off
	v_lshl_add_u64 v[196:197], s[82:83], 0, v[142:143]
	s_mov_b32 m0, s60
	s_nop 0
	global_load_lds_dwordx4 v[196:197], off
	s_waitcnt vmcnt(8)
	s_waitcnt lgkmcnt(0)
	s_barrier
	s_setprio 1
	s_waitcnt lgkmcnt(0)
	v_mfma_f32_16x16x128_f8f6f4 v[134:137], v[172:179], v[212:219], v[134:137]
	v_mfma_f32_16x16x128_f8f6f4 v[130:133], v[180:187], v[212:219], v[130:133]
	v_mfma_f32_16x16x128_f8f6f4 v[118:121], v[172:179], v[220:227], v[118:121]
	v_mfma_f32_16x16x128_f8f6f4 v[114:117], v[180:187], v[220:227], v[114:117]
	v_mfma_f32_16x16x128_f8f6f4 v[102:105], v[172:179], v[228:235], v[102:105]
	v_mfma_f32_16x16x128_f8f6f4 v[98:101], v[180:187], v[228:235], v[98:101]
	v_mfma_f32_16x16x128_f8f6f4 v[78:81], v[172:179], v[236:243], v[78:81]
	v_mfma_f32_16x16x128_f8f6f4 v[74:77], v[180:187], v[236:243], v[74:77]
	s_setprio 0
	s_setprio 1
	v_mfma_f32_16x16x128_f8f6f4 v[126:129], v[188:195], v[212:219], v[126:129]
	v_mfma_f32_16x16x128_f8f6f4 v[122:125], v[204:211], v[212:219], v[122:125]
	v_mfma_f32_16x16x128_f8f6f4 v[110:113], v[188:195], v[220:227], v[110:113]
	v_mfma_f32_16x16x128_f8f6f4 v[106:109], v[204:211], v[220:227], v[106:109]
	v_mfma_f32_16x16x128_f8f6f4 v[94:97], v[188:195], v[228:235], v[94:97]
	v_mfma_f32_16x16x128_f8f6f4 v[90:93], v[204:211], v[228:235], v[90:93]
	v_mfma_f32_16x16x128_f8f6f4 v[62:65], v[188:195], v[236:243], v[62:65]
	v_mfma_f32_16x16x128_f8f6f4 v[58:61], v[204:211], v[236:243], v[58:61]
	s_setprio 0
	s_barrier
	s_mov_b32 m0, s79
	v_lshl_add_u64 v[150:151], v[150:151], 0, s[34:35]
	s_add_u32 s72, s72, 0x8380
	ds_read_b128 v[212:215], v161 offset:49152
	ds_read_b128 v[216:219], v161 offset:50176
	ds_read_b128 v[220:223], v161 offset:51200
	ds_read_b128 v[224:227], v161 offset:52224
	ds_read_b128 v[228:231], v161 offset:53248
	ds_read_b128 v[232:235], v161 offset:54272
	ds_read_b128 v[236:239], v161 offset:55296
	ds_read_b128 v[240:243], v161 offset:56320
	global_load_lds_dwordx4 v[150:151], off
	v_lshl_add_u64 v[150:151], v[152:153], 0, s[34:35]
	s_mov_b32 m0, s39
	s_addc_u32 s73, s73, 0
	global_load_lds_dwordx4 v[150:151], off
	v_lshl_add_u64 v[150:151], s[72:73], 0, v[140:141]
	s_mov_b32 m0, s41
	s_nop 0
	global_load_lds_dwordx4 v[150:151], off
	v_lshl_add_u64 v[150:151], s[72:73], 0, v[144:145]
	s_mov_b32 m0, s71
	s_nop 0
	global_load_lds_dwordx4 v[150:151], off
	v_lshl_add_u64 v[150:151], v[154:155], 0, s[34:35]
	s_mov_b32 m0, s61
	s_nop 0
	global_load_lds_dwordx4 v[150:151], off
	v_lshl_add_u64 v[150:151], v[156:157], 0, s[34:35]
	s_mov_b32 m0, s62
	s_nop 0
	global_load_lds_dwordx4 v[150:151], off
	s_waitcnt vmcnt(8)
	s_waitcnt lgkmcnt(0)
	s_barrier
	s_setprio 1
	s_waitcnt lgkmcnt(0)
	v_mfma_f32_16x16x128_f8f6f4 v[86:89], v[172:179], v[212:219], v[86:89]
	v_mfma_f32_16x16x128_f8f6f4 v[82:85], v[180:187], v[212:219], v[82:85]
	v_mfma_f32_16x16x128_f8f6f4 v[54:57], v[172:179], v[220:227], v[54:57]
	v_mfma_f32_16x16x128_f8f6f4 v[50:53], v[180:187], v[220:227], v[50:53]
	v_mfma_f32_16x16x128_f8f6f4 v[38:41], v[172:179], v[228:235], v[38:41]
	v_mfma_f32_16x16x128_f8f6f4 v[34:37], v[180:187], v[228:235], v[34:37]
	v_mfma_f32_16x16x128_f8f6f4 v[22:25], v[172:179], v[236:243], v[22:25]
	v_mfma_f32_16x16x128_f8f6f4 v[18:21], v[180:187], v[236:243], v[18:21]
	s_setprio 0
	s_setprio 1
	v_mfma_f32_16x16x128_f8f6f4 v[70:73], v[188:195], v[212:219], v[70:73]
	v_mfma_f32_16x16x128_f8f6f4 v[66:69], v[204:211], v[212:219], v[66:69]
	v_mfma_f32_16x16x128_f8f6f4 v[46:49], v[188:195], v[220:227], v[46:49]
	v_mfma_f32_16x16x128_f8f6f4 v[42:45], v[204:211], v[220:227], v[42:45]
	v_mfma_f32_16x16x128_f8f6f4 v[30:33], v[188:195], v[228:235], v[30:33]
	v_mfma_f32_16x16x128_f8f6f4 v[26:29], v[204:211], v[228:235], v[26:29]
	v_mfma_f32_16x16x128_f8f6f4 v[14:17], v[188:195], v[236:243], v[14:17]
	v_mfma_f32_16x16x128_f8f6f4 v[10:13], v[204:211], v[236:243], v[10:13]
	s_setprio 0
	s_barrier
	ds_read_b128 v[150:153], v162
	ds_read_b128 v[154:157], v162 offset:1024
	ds_read_b128 v[172:175], v162 offset:2048
	ds_read_b128 v[176:179], v162 offset:3072
	ds_read_b128 v[180:183], v163
	ds_read_b128 v[184:187], v163 offset:1024
	ds_read_b128 v[188:191], v163 offset:2048
	ds_read_b128 v[192:195], v163 offset:3072
	s_add_u32 s68, s68, 0x20380
	s_addc_u32 s69, s69, 0
	s_mov_b32 m0, s63
	v_lshl_add_u64 v[196:197], s[68:69], 0, v[138:139]
	ds_read_b128 v[204:207], v161
	ds_read_b128 v[208:211], v161 offset:1024
	ds_read_b128 v[212:215], v161 offset:2048
	ds_read_b128 v[216:219], v161 offset:3072
	ds_read_b128 v[220:223], v161 offset:4096
	ds_read_b128 v[224:227], v161 offset:5120
	ds_read_b128 v[228:231], v161 offset:6144
	ds_read_b128 v[232:235], v161 offset:7168
	global_load_lds_dwordx4 v[196:197], off
	v_lshl_add_u64 v[196:197], s[68:69], 0, v[142:143]
	s_mov_b32 m0, s64
	s_nop 0
	global_load_lds_dwordx4 v[196:197], off
	s_waitcnt vmcnt(8)
	s_waitcnt lgkmcnt(0)
	s_barrier
	s_setprio 1
	s_waitcnt lgkmcnt(0)
	v_mfma_f32_16x16x128_f8f6f4 v[134:137], v[150:157], v[204:211], v[134:137]
	v_mfma_f32_16x16x128_f8f6f4 v[130:133], v[172:179], v[204:211], v[130:133]
	v_mfma_f32_16x16x128_f8f6f4 v[118:121], v[150:157], v[212:219], v[118:121]
	v_mfma_f32_16x16x128_f8f6f4 v[114:117], v[172:179], v[212:219], v[114:117]
	v_mfma_f32_16x16x128_f8f6f4 v[102:105], v[150:157], v[220:227], v[102:105]
	v_mfma_f32_16x16x128_f8f6f4 v[98:101], v[172:179], v[220:227], v[98:101]
	v_mfma_f32_16x16x128_f8f6f4 v[78:81], v[150:157], v[228:235], v[78:81]
	v_mfma_f32_16x16x128_f8f6f4 v[74:77], v[172:179], v[228:235], v[74:77]
	s_setprio 0
	s_setprio 1
	v_mfma_f32_16x16x128_f8f6f4 v[126:129], v[180:187], v[204:211], v[126:129]
	v_mfma_f32_16x16x128_f8f6f4 v[122:125], v[188:195], v[204:211], v[122:125]
	v_mfma_f32_16x16x128_f8f6f4 v[110:113], v[180:187], v[212:219], v[110:113]
	v_mfma_f32_16x16x128_f8f6f4 v[106:109], v[188:195], v[212:219], v[106:109]
	v_mfma_f32_16x16x128_f8f6f4 v[94:97], v[180:187], v[220:227], v[94:97]
	v_mfma_f32_16x16x128_f8f6f4 v[90:93], v[188:195], v[220:227], v[90:93]
	v_mfma_f32_16x16x128_f8f6f4 v[62:65], v[180:187], v[228:235], v[62:65]
	v_mfma_f32_16x16x128_f8f6f4 v[58:61], v[188:195], v[228:235], v[58:61]
	s_setprio 0
	s_barrier
	s_mov_b32 m0, s80
	v_lshl_add_u64 v[196:197], s[8:9], 0, v[140:141]
	s_add_u32 s68, s8, 0x8000
	ds_read_b128 v[204:207], v161 offset:16384
	ds_read_b128 v[208:211], v161 offset:17408
	ds_read_b128 v[212:215], v161 offset:18432
	ds_read_b128 v[216:219], v161 offset:19456
	ds_read_b128 v[220:223], v161 offset:20480
	ds_read_b128 v[224:227], v161 offset:21504
	ds_read_b128 v[228:231], v161 offset:22528
	ds_read_b128 v[232:235], v161 offset:23552
	global_load_lds_dwordx4 v[196:197], off
	v_lshl_add_u64 v[198:199], s[8:9], 0, v[144:145]
	s_mov_b32 m0, s76
	s_addc_u32 s69, s9, 0
	global_load_lds_dwordx4 v[198:199], off
	v_lshl_add_u64 v[200:201], s[68:69], 0, v[140:141]
	s_mov_b32 m0, s77
	v_lshl_add_u64 v[236:237], s[74:75], 0, v[142:143]
	global_load_lds_dwordx4 v[200:201], off
	v_lshl_add_u64 v[200:201], s[68:69], 0, v[144:145]
	s_mov_b32 m0, s78
	s_nop 0
	global_load_lds_dwordx4 v[200:201], off
	v_lshl_add_u64 v[200:201], s[74:75], 0, v[138:139]
	s_mov_b32 m0, s49
	s_nop 0
	global_load_lds_dwordx4 v[200:201], off
	s_mov_b32 m0, s51
	s_nop 0
	global_load_lds_dwordx4 v[236:237], off
	s_waitcnt vmcnt(8)
	s_waitcnt lgkmcnt(0)
	s_barrier
	s_setprio 1
	s_waitcnt lgkmcnt(0)
	v_mfma_f32_16x16x128_f8f6f4 v[86:89], v[150:157], v[204:211], v[86:89]
	v_mfma_f32_16x16x128_f8f6f4 v[82:85], v[172:179], v[204:211], v[82:85]
	v_mfma_f32_16x16x128_f8f6f4 v[54:57], v[150:157], v[212:219], v[54:57]
	v_mfma_f32_16x16x128_f8f6f4 v[50:53], v[172:179], v[212:219], v[50:53]
	v_mfma_f32_16x16x128_f8f6f4 v[38:41], v[150:157], v[220:227], v[38:41]
	v_mfma_f32_16x16x128_f8f6f4 v[34:37], v[172:179], v[220:227], v[34:37]
	v_mfma_f32_16x16x128_f8f6f4 v[22:25], v[150:157], v[228:235], v[22:25]
	v_mfma_f32_16x16x128_f8f6f4 v[18:21], v[172:179], v[228:235], v[18:21]
	s_setprio 0
	s_setprio 1
	v_mfma_f32_16x16x128_f8f6f4 v[70:73], v[180:187], v[204:211], v[70:73]
	v_mfma_f32_16x16x128_f8f6f4 v[66:69], v[188:195], v[204:211], v[66:69]
	v_mfma_f32_16x16x128_f8f6f4 v[46:49], v[180:187], v[212:219], v[46:49]
	v_mfma_f32_16x16x128_f8f6f4 v[42:45], v[188:195], v[212:219], v[42:45]
	v_mfma_f32_16x16x128_f8f6f4 v[30:33], v[180:187], v[220:227], v[30:33]
	v_mfma_f32_16x16x128_f8f6f4 v[26:29], v[188:195], v[220:227], v[26:29]
	v_mfma_f32_16x16x128_f8f6f4 v[14:17], v[180:187], v[228:235], v[14:17]
	v_mfma_f32_16x16x128_f8f6f4 v[10:13], v[188:195], v[228:235], v[10:13]
	s_setprio 0
	s_barrier
	ds_read_b128 v[150:153], v158
	ds_read_b128 v[154:157], v158 offset:1024
	ds_read_b128 v[172:175], v158 offset:2048
	ds_read_b128 v[176:179], v158 offset:3072
	ds_read_b128 v[180:183], v159
	ds_read_b128 v[184:187], v159 offset:1024
	ds_read_b128 v[188:191], v159 offset:2048
	ds_read_b128 v[192:195], v159 offset:3072
	s_add_u32 s68, s74, 0x20000
	s_addc_u32 s69, s75, 0
	s_mov_b32 m0, s59
	v_lshl_add_u64 v[158:159], s[68:69], 0, v[138:139]
	ds_read_b128 v[204:207], v161 offset:32768
	ds_read_b128 v[208:211], v161 offset:33792
	ds_read_b128 v[212:215], v161 offset:34816
	ds_read_b128 v[216:219], v161 offset:35840
	ds_read_b128 v[220:223], v161 offset:36864
	ds_read_b128 v[224:227], v161 offset:37888
	ds_read_b128 v[228:231], v161 offset:38912
	ds_read_b128 v[232:235], v161 offset:39936
	global_load_lds_dwordx4 v[158:159], off
	v_lshl_add_u64 v[158:159], s[68:69], 0, v[142:143]
	s_mov_b32 m0, s60
	s_nop 0
	global_load_lds_dwordx4 v[158:159], off
	s_waitcnt vmcnt(8)
	s_waitcnt lgkmcnt(0)
	s_barrier
	s_setprio 1
	s_waitcnt lgkmcnt(0)
	v_mfma_f32_16x16x128_f8f6f4 v[134:137], v[150:157], v[204:211], v[134:137]
	v_mfma_f32_16x16x128_f8f6f4 v[130:133], v[172:179], v[204:211], v[130:133]
	v_mfma_f32_16x16x128_f8f6f4 v[118:121], v[150:157], v[212:219], v[118:121]
	v_mfma_f32_16x16x128_f8f6f4 v[114:117], v[172:179], v[212:219], v[114:117]
	v_mfma_f32_16x16x128_f8f6f4 v[102:105], v[150:157], v[220:227], v[102:105]
	v_mfma_f32_16x16x128_f8f6f4 v[98:101], v[172:179], v[220:227], v[98:101]
	v_mfma_f32_16x16x128_f8f6f4 v[78:81], v[150:157], v[228:235], v[78:81]
	v_mfma_f32_16x16x128_f8f6f4 v[74:77], v[172:179], v[228:235], v[74:77]
	s_setprio 0
	s_setprio 1
	v_mfma_f32_16x16x128_f8f6f4 v[126:129], v[180:187], v[204:211], v[126:129]
	v_mfma_f32_16x16x128_f8f6f4 v[122:125], v[188:195], v[204:211], v[122:125]
	v_mfma_f32_16x16x128_f8f6f4 v[110:113], v[180:187], v[212:219], v[110:113]
	v_mfma_f32_16x16x128_f8f6f4 v[106:109], v[188:195], v[212:219], v[106:109]
	v_mfma_f32_16x16x128_f8f6f4 v[94:97], v[180:187], v[220:227], v[94:97]
	v_mfma_f32_16x16x128_f8f6f4 v[90:93], v[188:195], v[220:227], v[90:93]
	v_mfma_f32_16x16x128_f8f6f4 v[62:65], v[180:187], v[228:235], v[62:65]
	v_mfma_f32_16x16x128_f8f6f4 v[58:61], v[188:195], v[228:235], v[58:61]
	s_setprio 0
	s_barrier
	s_mov_b32 m0, s79
	v_lshl_add_u64 v[158:159], v[196:197], 0, s[18:19]
	s_add_u32 s8, s8, 0x8080
	ds_read_b128 v[204:207], v161 offset:49152
	ds_read_b128 v[208:211], v161 offset:50176
	ds_read_b128 v[212:215], v161 offset:51200
	ds_read_b128 v[216:219], v161 offset:52224
	ds_read_b128 v[220:223], v161 offset:53248
	ds_read_b128 v[224:227], v161 offset:54272
	ds_read_b128 v[228:231], v161 offset:55296
	ds_read_b128 v[232:235], v161 offset:56320
	global_load_lds_dwordx4 v[158:159], off
	v_lshl_add_u64 v[158:159], v[198:199], 0, s[18:19]
	s_mov_b32 m0, s39
	s_addc_u32 s9, s9, 0
	global_load_lds_dwordx4 v[158:159], off
	v_lshl_add_u64 v[158:159], s[8:9], 0, v[140:141]
	s_mov_b32 m0, s41
	s_nop 0
	global_load_lds_dwordx4 v[158:159], off
	v_lshl_add_u64 v[158:159], s[8:9], 0, v[144:145]
	s_mov_b32 m0, s71
	s_nop 0
	global_load_lds_dwordx4 v[158:159], off
	v_lshl_add_u64 v[158:159], v[200:201], 0, s[18:19]
	s_mov_b32 m0, s61
	s_nop 0
	global_load_lds_dwordx4 v[158:159], off
	v_lshl_add_u64 v[158:159], v[236:237], 0, s[18:19]
	s_mov_b32 m0, s62
	s_nop 0
	global_load_lds_dwordx4 v[158:159], off
	s_waitcnt vmcnt(8)
	s_waitcnt lgkmcnt(0)
	s_barrier
	s_setprio 1
	s_waitcnt lgkmcnt(0)
	v_mfma_f32_16x16x128_f8f6f4 v[86:89], v[150:157], v[204:211], v[86:89]
	v_mfma_f32_16x16x128_f8f6f4 v[82:85], v[172:179], v[204:211], v[82:85]
	v_mfma_f32_16x16x128_f8f6f4 v[54:57], v[150:157], v[212:219], v[54:57]
	v_mfma_f32_16x16x128_f8f6f4 v[50:53], v[172:179], v[212:219], v[50:53]
	v_mfma_f32_16x16x128_f8f6f4 v[38:41], v[150:157], v[220:227], v[38:41]
	v_mfma_f32_16x16x128_f8f6f4 v[34:37], v[172:179], v[220:227], v[34:37]
	v_mfma_f32_16x16x128_f8f6f4 v[22:25], v[150:157], v[228:235], v[22:25]
	v_mfma_f32_16x16x128_f8f6f4 v[18:21], v[172:179], v[228:235], v[18:21]
	s_setprio 0
	s_setprio 1
	v_mfma_f32_16x16x128_f8f6f4 v[70:73], v[180:187], v[204:211], v[70:73]
	v_mfma_f32_16x16x128_f8f6f4 v[66:69], v[188:195], v[204:211], v[66:69]
	v_mfma_f32_16x16x128_f8f6f4 v[46:49], v[180:187], v[212:219], v[46:49]
	v_mfma_f32_16x16x128_f8f6f4 v[42:45], v[188:195], v[212:219], v[42:45]
	v_mfma_f32_16x16x128_f8f6f4 v[30:33], v[180:187], v[220:227], v[30:33]
	v_mfma_f32_16x16x128_f8f6f4 v[26:29], v[188:195], v[220:227], v[26:29]
	v_mfma_f32_16x16x128_f8f6f4 v[14:17], v[180:187], v[228:235], v[14:17]
	v_mfma_f32_16x16x128_f8f6f4 v[10:13], v[188:195], v[228:235], v[10:13]
	s_setprio 0
	s_barrier
	v_cndmask_b32_e64 v150, 0, 1, s[6:7]
	v_cmp_ne_u32_e64 s[8:9], 1, v150
	s_andn2_b64 vcc, exec, s[6:7]
	s_cbranch_vccnz .LBB0_1625
	s_add_u32 s6, s44, 0x20080
	s_addc_u32 s7, s45, 0
	s_mov_b32 m0, s63
	v_lshl_add_u64 v[150:151], s[6:7], 0, v[138:139]
	v_lshl_add_u64 v[152:153], s[6:7], 0, v[142:143]
	global_load_lds_dwordx4 v[150:151], off
	s_mov_b32 m0, s64
	s_nop 0
	global_load_lds_dwordx4 v[152:153], off

.LBB0_3425:
	s_ashr_i32 s43, s42, 31
	s_lshl_b64 s[10:11], s[42:43], 18
	s_add_u32 s46, s6, s10
	ds_read_b128 v[10:13], v162
	ds_read_b128 v[14:17], v162 offset:1024
	ds_read_b128 v[26:29], v162 offset:2048
	ds_read_b128 v[30:33], v162 offset:3072
	ds_read_b128 v[172:175], v163
	ds_read_b128 v[176:179], v163 offset:1024
	ds_read_b128 v[180:183], v163 offset:2048
	ds_read_b128 v[184:187], v163 offset:3072
	s_addc_u32 s47, s7, s11
	s_and_b64 s[10:11], s[8:9], exec
	s_cselect_b32 s71, s47, s65
	s_cselect_b32 s70, s46, s64
	s_ashr_i32 s45, s44, 31
	s_ashr_i32 s41, s40, 31
	s_lshl_b64 s[10:11], s[44:45], 20
	s_lshl_b64 s[48:49], s[40:41], 18
	s_add_u32 s10, s33, s10
	s_addc_u32 s11, s39, s11
	s_add_u32 s48, s10, s48
	s_addc_u32 s49, s11, s49
	s_and_b64 s[10:11], s[8:9], exec
	s_cselect_b32 s11, s49, s67
	s_cselect_b32 s10, s48, s66
	ds_read_b128 v[18:21], v161
	ds_read_b128 v[22:25], v161 offset:1024
	ds_read_b128 v[34:37], v161 offset:2048
	ds_read_b128 v[38:41], v161 offset:3072
	ds_read_b128 v[42:45], v161 offset:4096
	ds_read_b128 v[46:49], v161 offset:5120
	ds_read_b128 v[50:53], v161 offset:6144
	ds_read_b128 v[54:57], v161 offset:7168
	s_waitcnt vmcnt(26)
	s_waitcnt lgkmcnt(0)
	s_barrier
	s_setprio 1
	s_waitcnt lgkmcnt(0)
	v_mfma_f32_16x16x128_f8f6f4 v[134:137], v[10:17], v[18:25], 0
	v_mfma_f32_16x16x128_f8f6f4 v[130:133], v[26:33], v[18:25], 0
	v_mfma_f32_16x16x128_f8f6f4 v[118:121], v[10:17], v[34:41], 0
	v_mfma_f32_16x16x128_f8f6f4 v[114:117], v[26:33], v[34:41], 0
	v_mfma_f32_16x16x128_f8f6f4 v[102:105], v[10:17], v[42:49], 0
	v_mfma_f32_16x16x128_f8f6f4 v[98:101], v[26:33], v[42:49], 0
	v_mfma_f32_16x16x128_f8f6f4 v[78:81], v[10:17], v[50:57], 0
	v_mfma_f32_16x16x128_f8f6f4 v[74:77], v[26:33], v[50:57], 0
	s_setprio 0
	s_setprio 1
	v_mfma_f32_16x16x128_f8f6f4 v[126:129], v[172:179], v[18:25], 0
	v_mfma_f32_16x16x128_f8f6f4 v[122:125], v[180:187], v[18:25], 0
	v_mfma_f32_16x16x128_f8f6f4 v[110:113], v[172:179], v[34:41], 0
	v_mfma_f32_16x16x128_f8f6f4 v[106:109], v[180:187], v[34:41], 0
	v_mfma_f32_16x16x128_f8f6f4 v[94:97], v[172:179], v[42:49], 0
	v_mfma_f32_16x16x128_f8f6f4 v[90:93], v[180:187], v[42:49], 0
	v_mfma_f32_16x16x128_f8f6f4 v[62:65], v[172:179], v[50:57], 0
	v_mfma_f32_16x16x128_f8f6f4 v[58:61], v[180:187], v[50:57], 0
	s_setprio 0
	s_barrier
	s_add_i32 s80, s73, s56
	v_lshl_add_u64 v[150:151], s[66:67], 0, v[140:141]
	s_add_i32 s76, s80, 0x2000
	v_lshl_add_u64 v[18:19], v[150:151], 0, s[24:25]
	s_mov_b32 m0, s80
	v_lshl_add_u64 v[152:153], s[66:67], 0, v[144:145]
	s_add_u32 s78, s66, 0x8100
	ds_read_b128 v[42:45], v161 offset:16384
	ds_read_b128 v[46:49], v161 offset:17408
	ds_read_b128 v[188:191], v161 offset:18432
	ds_read_b128 v[192:195], v161 offset:19456
	ds_read_b128 v[204:207], v161 offset:20480
	ds_read_b128 v[208:211], v161 offset:21504
	ds_read_b128 v[212:215], v161 offset:22528
	ds_read_b128 v[216:219], v161 offset:23552
	global_load_lds_dwordx4 v[18:19], off
	v_lshl_add_u64 v[18:19], v[152:153], 0, s[24:25]
	s_mov_b32 m0, s76
	s_addc_u32 s79, s67, 0
	s_add_i32 s77, s74, s56
	global_load_lds_dwordx4 v[18:19], off
	v_lshl_add_u64 v[18:19], s[78:79], 0, v[140:141]
	s_mov_b32 m0, s77
	v_lshl_add_u64 v[154:155], s[64:65], 0, v[138:139]
	global_load_lds_dwordx4 v[18:19], off
	v_lshl_add_u64 v[18:19], s[78:79], 0, v[144:145]
	s_add_i32 s78, s77, 0x2000
	s_mov_b32 m0, s78
	v_lshl_add_u64 v[156:157], s[64:65], 0, v[142:143]
	global_load_lds_dwordx4 v[18:19], off
	v_lshl_add_u64 v[18:19], v[154:155], 0, s[24:25]
	s_mov_b32 m0, s51
	s_nop 0
	global_load_lds_dwordx4 v[18:19], off
	v_lshl_add_u64 v[18:19], v[156:157], 0, s[24:25]
	s_mov_b32 m0, s57
	s_nop 0
	global_load_lds_dwordx4 v[18:19], off
	s_waitcnt vmcnt(26)
	s_waitcnt lgkmcnt(0)
	s_barrier
	s_setprio 1
	s_waitcnt lgkmcnt(0)
	v_mfma_f32_16x16x128_f8f6f4 v[86:89], v[10:17], v[42:49], 0
	v_mfma_f32_16x16x128_f8f6f4 v[82:85], v[26:33], v[42:49], 0
	v_mfma_f32_16x16x128_f8f6f4 v[54:57], v[10:17], v[188:195], 0
	v_mfma_f32_16x16x128_f8f6f4 v[50:53], v[26:33], v[188:195], 0
	v_mfma_f32_16x16x128_f8f6f4 v[38:41], v[10:17], v[204:211], 0
	v_mfma_f32_16x16x128_f8f6f4 v[34:37], v[26:33], v[204:211], 0
	v_mfma_f32_16x16x128_f8f6f4 v[22:25], v[10:17], v[212:219], 0
	v_mfma_f32_16x16x128_f8f6f4 v[18:21], v[26:33], v[212:219], 0
	s_setprio 0
	s_setprio 1
	v_mfma_f32_16x16x128_f8f6f4 v[70:73], v[172:179], v[42:49], 0
	v_mfma_f32_16x16x128_f8f6f4 v[66:69], v[180:187], v[42:49], 0
	v_mfma_f32_16x16x128_f8f6f4 v[46:49], v[172:179], v[188:195], 0
	v_mfma_f32_16x16x128_f8f6f4 v[42:45], v[180:187], v[188:195], 0
	v_mfma_f32_16x16x128_f8f6f4 v[30:33], v[172:179], v[204:211], 0
	v_mfma_f32_16x16x128_f8f6f4 v[26:29], v[180:187], v[204:211], 0
	v_mfma_f32_16x16x128_f8f6f4 v[14:17], v[172:179], v[212:219], 0
	v_mfma_f32_16x16x128_f8f6f4 v[10:13], v[180:187], v[212:219], 0
	s_setprio 0
	s_barrier
	s_add_i32 s79, 0, 0x18000
	s_add_i32 s43, 0, 0x1c000
	v_add_u32_e32 v158, s79, v160
	v_add_u32_e32 v159, s43, v160
	ds_read_b128 v[172:175], v158
	ds_read_b128 v[176:179], v158 offset:1024
	ds_read_b128 v[180:183], v158 offset:2048
	ds_read_b128 v[184:187], v158 offset:3072
	ds_read_b128 v[188:191], v159
	ds_read_b128 v[192:195], v159 offset:1024
	ds_read_b128 v[204:207], v159 offset:2048
	ds_read_b128 v[208:211], v159 offset:3072
	s_add_u32 s82, s64, 0x20100
	s_addc_u32 s83, s65, 0
	s_mov_b32 m0, s58
	v_lshl_add_u64 v[196:197], s[82:83], 0, v[138:139]
	ds_read_b128 v[212:215], v161 offset:32768
	ds_read_b128 v[216:219], v161 offset:33792
	ds_read_b128 v[220:223], v161 offset:34816
	ds_read_b128 v[224:227], v161 offset:35840
	ds_read_b128 v[228:231], v161 offset:36864
	ds_read_b128 v[232:235], v161 offset:37888
	ds_read_b128 v[236:239], v161 offset:38912
	ds_read_b128 v[240:243], v161 offset:39936
	global_load_lds_dwordx4 v[196:197], off
	v_lshl_add_u64 v[196:197], s[82:83], 0, v[142:143]
	s_mov_b32 m0, s59
	s_nop 0
	global_load_lds_dwordx4 v[196:197], off
	s_waitcnt vmcnt(26)
	s_waitcnt lgkmcnt(0)
	s_barrier
	s_setprio 1
	s_waitcnt lgkmcnt(0)
	v_mfma_f32_16x16x128_f8f6f4 v[134:137], v[172:179], v[212:219], v[134:137]
	v_mfma_f32_16x16x128_f8f6f4 v[130:133], v[180:187], v[212:219], v[130:133]
	v_mfma_f32_16x16x128_f8f6f4 v[118:121], v[172:179], v[220:227], v[118:121]
	v_mfma_f32_16x16x128_f8f6f4 v[114:117], v[180:187], v[220:227], v[114:117]
	v_mfma_f32_16x16x128_f8f6f4 v[102:105], v[172:179], v[228:235], v[102:105]
	v_mfma_f32_16x16x128_f8f6f4 v[98:101], v[180:187], v[228:235], v[98:101]
	v_mfma_f32_16x16x128_f8f6f4 v[78:81], v[172:179], v[236:243], v[78:81]
	v_mfma_f32_16x16x128_f8f6f4 v[74:77], v[180:187], v[236:243], v[74:77]
	s_setprio 0
	s_setprio 1
	v_mfma_f32_16x16x128_f8f6f4 v[126:129], v[188:195], v[212:219], v[126:129]
	v_mfma_f32_16x16x128_f8f6f4 v[122:125], v[204:211], v[212:219], v[122:125]
	v_mfma_f32_16x16x128_f8f6f4 v[110:113], v[188:195], v[220:227], v[110:113]
	v_mfma_f32_16x16x128_f8f6f4 v[106:109], v[204:211], v[220:227], v[106:109]
	v_mfma_f32_16x16x128_f8f6f4 v[94:97], v[188:195], v[228:235], v[94:97]
	v_mfma_f32_16x16x128_f8f6f4 v[90:93], v[204:211], v[228:235], v[90:93]
	v_mfma_f32_16x16x128_f8f6f4 v[62:65], v[188:195], v[236:243], v[62:65]
	v_mfma_f32_16x16x128_f8f6f4 v[58:61], v[204:211], v[236:243], v[58:61]
	s_setprio 0
	s_barrier
	s_add_i32 s79, s79, s56
	s_add_i32 s41, s79, 0x2000
	v_lshl_add_u64 v[196:197], v[150:151], 0, s[26:27]
	s_mov_b32 m0, s79
	s_add_u32 s82, s66, 0x8180
	ds_read_b128 v[212:215], v161 offset:49152
	ds_read_b128 v[216:219], v161 offset:50176
	ds_read_b128 v[220:223], v161 offset:51200
	ds_read_b128 v[224:227], v161 offset:52224
	ds_read_b128 v[228:231], v161 offset:53248
	ds_read_b128 v[232:235], v161 offset:54272
	ds_read_b128 v[236:239], v161 offset:55296
	ds_read_b128 v[240:243], v161 offset:56320
	global_load_lds_dwordx4 v[196:197], off
	v_lshl_add_u64 v[196:197], v[152:153], 0, s[26:27]
	s_mov_b32 m0, s41
	s_addc_u32 s83, s67, 0
	s_add_i32 s43, s43, s56
	global_load_lds_dwordx4 v[196:197], off
	v_lshl_add_u64 v[196:197], s[82:83], 0, v[140:141]
	s_mov_b32 m0, s43
	s_add_i32 s68, s43, 0x2000
	global_load_lds_dwordx4 v[196:197], off
	v_lshl_add_u64 v[196:197], s[82:83], 0, v[144:145]
	s_mov_b32 m0, s68
	s_nop 0
	global_load_lds_dwordx4 v[196:197], off
	v_lshl_add_u64 v[196:197], v[154:155], 0, s[26:27]
	s_mov_b32 m0, s60
	s_nop 0
	global_load_lds_dwordx4 v[196:197], off
	v_lshl_add_u64 v[196:197], v[156:157], 0, s[26:27]
	s_mov_b32 m0, s61
	s_nop 0
	global_load_lds_dwordx4 v[196:197], off
	s_waitcnt vmcnt(8)
	s_waitcnt lgkmcnt(0)
	s_barrier
	s_setprio 1
	s_waitcnt lgkmcnt(0)
	v_mfma_f32_16x16x128_f8f6f4 v[86:89], v[172:179], v[212:219], v[86:89]
	v_mfma_f32_16x16x128_f8f6f4 v[82:85], v[180:187], v[212:219], v[82:85]
	v_mfma_f32_16x16x128_f8f6f4 v[54:57], v[172:179], v[220:227], v[54:57]
	v_mfma_f32_16x16x128_f8f6f4 v[50:53], v[180:187], v[220:227], v[50:53]
	v_mfma_f32_16x16x128_f8f6f4 v[38:41], v[172:179], v[228:235], v[38:41]
	v_mfma_f32_16x16x128_f8f6f4 v[34:37], v[180:187], v[228:235], v[34:37]
	v_mfma_f32_16x16x128_f8f6f4 v[22:25], v[172:179], v[236:243], v[22:25]
	v_mfma_f32_16x16x128_f8f6f4 v[18:21], v[180:187], v[236:243], v[18:21]
	s_setprio 0
	s_setprio 1
	v_mfma_f32_16x16x128_f8f6f4 v[70:73], v[188:195], v[212:219], v[70:73]
	v_mfma_f32_16x16x128_f8f6f4 v[66:69], v[204:211], v[212:219], v[66:69]
	v_mfma_f32_16x16x128_f8f6f4 v[46:49], v[188:195], v[220:227], v[46:49]
	v_mfma_f32_16x16x128_f8f6f4 v[42:45], v[204:211], v[220:227], v[42:45]
	v_mfma_f32_16x16x128_f8f6f4 v[30:33], v[188:195], v[228:235], v[30:33]
	v_mfma_f32_16x16x128_f8f6f4 v[26:29], v[204:211], v[228:235], v[26:29]
	v_mfma_f32_16x16x128_f8f6f4 v[14:17], v[188:195], v[236:243], v[14:17]
	v_mfma_f32_16x16x128_f8f6f4 v[10:13], v[204:211], v[236:243], v[10:13]
	s_setprio 0
	s_barrier
	ds_read_b128 v[172:175], v162
	ds_read_b128 v[176:179], v162 offset:1024
	ds_read_b128 v[180:183], v162 offset:2048
	ds_read_b128 v[184:187], v162 offset:3072
	ds_read_b128 v[188:191], v163
	ds_read_b128 v[192:195], v163 offset:1024
	ds_read_b128 v[204:207], v163 offset:2048
	ds_read_b128 v[208:211], v163 offset:3072
	s_add_u32 s82, s64, 0x20180
	s_addc_u32 s83, s65, 0
	s_mov_b32 m0, s63
	v_lshl_add_u64 v[196:197], s[82:83], 0, v[138:139]
	ds_read_b128 v[212:215], v161
	ds_read_b128 v[216:219], v161 offset:1024
	ds_read_b128 v[220:223], v161 offset:2048
	ds_read_b128 v[224:227], v161 offset:3072
	ds_read_b128 v[228:231], v161 offset:4096
	ds_read_b128 v[232:235], v161 offset:5120
	ds_read_b128 v[236:239], v161 offset:6144
	ds_read_b128 v[240:243], v161 offset:7168
	global_load_lds_dwordx4 v[196:197], off
	v_lshl_add_u64 v[196:197], s[82:83], 0, v[142:143]
	s_mov_b32 m0, s69
	s_nop 0
	global_load_lds_dwordx4 v[196:197], off
	s_waitcnt vmcnt(8)
	s_waitcnt lgkmcnt(0)
	s_barrier
	s_setprio 1
	s_waitcnt lgkmcnt(0)
	v_mfma_f32_16x16x128_f8f6f4 v[134:137], v[172:179], v[212:219], v[134:137]
	v_mfma_f32_16x16x128_f8f6f4 v[130:133], v[180:187], v[212:219], v[130:133]
	v_mfma_f32_16x16x128_f8f6f4 v[118:121], v[172:179], v[220:227], v[118:121]
	v_mfma_f32_16x16x128_f8f6f4 v[114:117], v[180:187], v[220:227], v[114:117]
	v_mfma_f32_16x16x128_f8f6f4 v[102:105], v[172:179], v[228:235], v[102:105]
	v_mfma_f32_16x16x128_f8f6f4 v[98:101], v[180:187], v[228:235], v[98:101]
	v_mfma_f32_16x16x128_f8f6f4 v[78:81], v[172:179], v[236:243], v[78:81]
	v_mfma_f32_16x16x128_f8f6f4 v[74:77], v[180:187], v[236:243], v[74:77]
	s_setprio 0
	s_setprio 1
	v_mfma_f32_16x16x128_f8f6f4 v[126:129], v[188:195], v[212:219], v[126:129]
	v_mfma_f32_16x16x128_f8f6f4 v[122:125], v[204:211], v[212:219], v[122:125]
	v_mfma_f32_16x16x128_f8f6f4 v[110:113], v[188:195], v[220:227], v[110:113]
	v_mfma_f32_16x16x128_f8f6f4 v[106:109], v[204:211], v[220:227], v[106:109]
	v_mfma_f32_16x16x128_f8f6f4 v[94:97], v[188:195], v[228:235], v[94:97]
	v_mfma_f32_16x16x128_f8f6f4 v[90:93], v[204:211], v[228:235], v[90:93]
	v_mfma_f32_16x16x128_f8f6f4 v[62:65], v[188:195], v[236:243], v[62:65]
	v_mfma_f32_16x16x128_f8f6f4 v[58:61], v[204:211], v[236:243], v[58:61]
	s_setprio 0
	s_barrier
	s_mov_b32 m0, s80
	v_lshl_add_u64 v[196:197], v[150:151], 0, s[28:29]
	s_add_u32 s82, s66, 0x8200
	ds_read_b128 v[212:215], v161 offset:16384
	ds_read_b128 v[216:219], v161 offset:17408
	ds_read_b128 v[220:223], v161 offset:18432
	ds_read_b128 v[224:227], v161 offset:19456
	ds_read_b128 v[228:231], v161 offset:20480
	ds_read_b128 v[232:235], v161 offset:21504
	ds_read_b128 v[236:239], v161 offset:22528
	ds_read_b128 v[240:243], v161 offset:23552
	global_load_lds_dwordx4 v[196:197], off
	v_lshl_add_u64 v[196:197], v[152:153], 0, s[28:29]
	s_mov_b32 m0, s76
	s_addc_u32 s83, s67, 0
	global_load_lds_dwordx4 v[196:197], off
	v_lshl_add_u64 v[196:197], s[82:83], 0, v[140:141]
	s_mov_b32 m0, s77
	s_nop 0
	global_load_lds_dwordx4 v[196:197], off
	v_lshl_add_u64 v[196:197], s[82:83], 0, v[144:145]
	s_mov_b32 m0, s78
	s_nop 0
	global_load_lds_dwordx4 v[196:197], off
	v_lshl_add_u64 v[196:197], v[154:155], 0, s[28:29]
	s_mov_b32 m0, s51
	s_nop 0
	global_load_lds_dwordx4 v[196:197], off
	v_lshl_add_u64 v[196:197], v[156:157], 0, s[28:29]
	s_mov_b32 m0, s57
	s_nop 0
	global_load_lds_dwordx4 v[196:197], off
	s_waitcnt vmcnt(8)
	s_waitcnt lgkmcnt(0)
	s_barrier
	s_setprio 1
	s_waitcnt lgkmcnt(0)
	v_mfma_f32_16x16x128_f8f6f4 v[86:89], v[172:179], v[212:219], v[86:89]
	v_mfma_f32_16x16x128_f8f6f4 v[82:85], v[180:187], v[212:219], v[82:85]
	v_mfma_f32_16x16x128_f8f6f4 v[54:57], v[172:179], v[220:227], v[54:57]
	v_mfma_f32_16x16x128_f8f6f4 v[50:53], v[180:187], v[220:227], v[50:53]
	v_mfma_f32_16x16x128_f8f6f4 v[38:41], v[172:179], v[228:235], v[38:41]
	v_mfma_f32_16x16x128_f8f6f4 v[34:37], v[180:187], v[228:235], v[34:37]
	v_mfma_f32_16x16x128_f8f6f4 v[22:25], v[172:179], v[236:243], v[22:25]
	v_mfma_f32_16x16x128_f8f6f4 v[18:21], v[180:187], v[236:243], v[18:21]
	s_setprio 0
	s_setprio 1
	v_mfma_f32_16x16x128_f8f6f4 v[70:73], v[188:195], v[212:219], v[70:73]
	v_mfma_f32_16x16x128_f8f6f4 v[66:69], v[204:211], v[212:219], v[66:69]
	v_mfma_f32_16x16x128_f8f6f4 v[46:49], v[188:195], v[220:227], v[46:49]
	v_mfma_f32_16x16x128_f8f6f4 v[42:45], v[204:211], v[220:227], v[42:45]
	v_mfma_f32_16x16x128_f8f6f4 v[30:33], v[188:195], v[228:235], v[30:33]
	v_mfma_f32_16x16x128_f8f6f4 v[26:29], v[204:211], v[228:235], v[26:29]
	v_mfma_f32_16x16x128_f8f6f4 v[14:17], v[188:195], v[236:243], v[14:17]
	v_mfma_f32_16x16x128_f8f6f4 v[10:13], v[204:211], v[236:243], v[10:13]
	s_setprio 0
	s_barrier
	ds_read_b128 v[172:175], v158
	ds_read_b128 v[176:179], v158 offset:1024
	ds_read_b128 v[180:183], v158 offset:2048
	ds_read_b128 v[184:187], v158 offset:3072
	ds_read_b128 v[188:191], v159
	ds_read_b128 v[192:195], v159 offset:1024
	ds_read_b128 v[204:207], v159 offset:2048
	ds_read_b128 v[208:211], v159 offset:3072
	s_add_u32 s82, s64, 0x20200
	s_addc_u32 s83, s65, 0
	s_mov_b32 m0, s58
	v_lshl_add_u64 v[196:197], s[82:83], 0, v[138:139]
	ds_read_b128 v[212:215], v161 offset:32768
	ds_read_b128 v[216:219], v161 offset:33792
	ds_read_b128 v[220:223], v161 offset:34816
	ds_read_b128 v[224:227], v161 offset:35840
	ds_read_b128 v[228:231], v161 offset:36864
	ds_read_b128 v[232:235], v161 offset:37888
	ds_read_b128 v[236:239], v161 offset:38912
	ds_read_b128 v[240:243], v161 offset:39936
	global_load_lds_dwordx4 v[196:197], off
	v_lshl_add_u64 v[196:197], s[82:83], 0, v[142:143]
	s_mov_b32 m0, s59
	s_nop 0
	global_load_lds_dwordx4 v[196:197], off
	s_waitcnt vmcnt(8)
	s_waitcnt lgkmcnt(0)
	s_barrier
	s_setprio 1
	s_waitcnt lgkmcnt(0)
	v_mfma_f32_16x16x128_f8f6f4 v[134:137], v[172:179], v[212:219], v[134:137]
	v_mfma_f32_16x16x128_f8f6f4 v[130:133], v[180:187], v[212:219], v[130:133]
	v_mfma_f32_16x16x128_f8f6f4 v[118:121], v[172:179], v[220:227], v[118:121]
	v_mfma_f32_16x16x128_f8f6f4 v[114:117], v[180:187], v[220:227], v[114:117]
	v_mfma_f32_16x16x128_f8f6f4 v[102:105], v[172:179], v[228:235], v[102:105]
	v_mfma_f32_16x16x128_f8f6f4 v[98:101], v[180:187], v[228:235], v[98:101]
	v_mfma_f32_16x16x128_f8f6f4 v[78:81], v[172:179], v[236:243], v[78:81]
	v_mfma_f32_16x16x128_f8f6f4 v[74:77], v[180:187], v[236:243], v[74:77]
	s_setprio 0
	s_setprio 1
	v_mfma_f32_16x16x128_f8f6f4 v[126:129], v[188:195], v[212:219], v[126:129]
	v_mfma_f32_16x16x128_f8f6f4 v[122:125], v[204:211], v[212:219], v[122:125]
	v_mfma_f32_16x16x128_f8f6f4 v[110:113], v[188:195], v[220:227], v[110:113]
	v_mfma_f32_16x16x128_f8f6f4 v[106:109], v[204:211], v[220:227], v[106:109]
	v_mfma_f32_16x16x128_f8f6f4 v[94:97], v[188:195], v[228:235], v[94:97]
	v_mfma_f32_16x16x128_f8f6f4 v[90:93], v[204:211], v[228:235], v[90:93]
	v_mfma_f32_16x16x128_f8f6f4 v[62:65], v[188:195], v[236:243], v[62:65]
	v_mfma_f32_16x16x128_f8f6f4 v[58:61], v[204:211], v[236:243], v[58:61]
	s_setprio 0
	s_barrier
	s_mov_b32 m0, s79
	v_lshl_add_u64 v[196:197], v[150:151], 0, s[30:31]
	s_add_u32 s82, s66, 0x8280
	ds_read_b128 v[212:215], v161 offset:49152
	ds_read_b128 v[216:219], v161 offset:50176
	ds_read_b128 v[220:223], v161 offset:51200
	ds_read_b128 v[224:227], v161 offset:52224
	ds_read_b128 v[228:231], v161 offset:53248
	ds_read_b128 v[232:235], v161 offset:54272
	ds_read_b128 v[236:239], v161 offset:55296
	ds_read_b128 v[240:243], v161 offset:56320
	global_load_lds_dwordx4 v[196:197], off
	v_lshl_add_u64 v[196:197], v[152:153], 0, s[30:31]
	s_mov_b32 m0, s41
	s_addc_u32 s83, s67, 0
	global_load_lds_dwordx4 v[196:197], off
	v_lshl_add_u64 v[196:197], s[82:83], 0, v[140:141]
	s_mov_b32 m0, s43
	s_nop 0
	global_load_lds_dwordx4 v[196:197], off
	v_lshl_add_u64 v[196:197], s[82:83], 0, v[144:145]
	s_mov_b32 m0, s68
	s_nop 0
	global_load_lds_dwordx4 v[196:197], off
	v_lshl_add_u64 v[196:197], v[154:155], 0, s[30:31]
	s_mov_b32 m0, s60
	s_nop 0
	global_load_lds_dwordx4 v[196:197], off
	v_lshl_add_u64 v[196:197], v[156:157], 0, s[30:31]
	s_mov_b32 m0, s61
	s_nop 0
	global_load_lds_dwordx4 v[196:197], off
	s_waitcnt vmcnt(8)
	s_waitcnt lgkmcnt(0)
	s_barrier
	s_setprio 1
	s_waitcnt lgkmcnt(0)
	v_mfma_f32_16x16x128_f8f6f4 v[86:89], v[172:179], v[212:219], v[86:89]
	v_mfma_f32_16x16x128_f8f6f4 v[82:85], v[180:187], v[212:219], v[82:85]
	v_mfma_f32_16x16x128_f8f6f4 v[54:57], v[172:179], v[220:227], v[54:57]
	v_mfma_f32_16x16x128_f8f6f4 v[50:53], v[180:187], v[220:227], v[50:53]
	v_mfma_f32_16x16x128_f8f6f4 v[38:41], v[172:179], v[228:235], v[38:41]
	v_mfma_f32_16x16x128_f8f6f4 v[34:37], v[180:187], v[228:235], v[34:37]
	v_mfma_f32_16x16x128_f8f6f4 v[22:25], v[172:179], v[236:243], v[22:25]
	v_mfma_f32_16x16x128_f8f6f4 v[18:21], v[180:187], v[236:243], v[18:21]
	s_setprio 0
	s_setprio 1
	v_mfma_f32_16x16x128_f8f6f4 v[70:73], v[188:195], v[212:219], v[70:73]
	v_mfma_f32_16x16x128_f8f6f4 v[66:69], v[204:211], v[212:219], v[66:69]
	v_mfma_f32_16x16x128_f8f6f4 v[46:49], v[188:195], v[220:227], v[46:49]
	v_mfma_f32_16x16x128_f8f6f4 v[42:45], v[204:211], v[220:227], v[42:45]
	v_mfma_f32_16x16x128_f8f6f4 v[30:33], v[188:195], v[228:235], v[30:33]
	v_mfma_f32_16x16x128_f8f6f4 v[26:29], v[204:211], v[228:235], v[26:29]
	v_mfma_f32_16x16x128_f8f6f4 v[14:17], v[188:195], v[236:243], v[14:17]
	v_mfma_f32_16x16x128_f8f6f4 v[10:13], v[204:211], v[236:243], v[10:13]
	s_setprio 0
	s_barrier
	ds_read_b128 v[172:175], v162
	ds_read_b128 v[176:179], v162 offset:1024
	ds_read_b128 v[180:183], v162 offset:2048
	ds_read_b128 v[184:187], v162 offset:3072
	ds_read_b128 v[188:191], v163
	ds_read_b128 v[192:195], v163 offset:1024
	ds_read_b128 v[204:207], v163 offset:2048
	ds_read_b128 v[208:211], v163 offset:3072
	s_add_u32 s82, s64, 0x20280
	s_addc_u32 s83, s65, 0
	s_mov_b32 m0, s63
	v_lshl_add_u64 v[196:197], s[82:83], 0, v[138:139]
	ds_read_b128 v[212:215], v161
	ds_read_b128 v[216:219], v161 offset:1024
	ds_read_b128 v[220:223], v161 offset:2048
	ds_read_b128 v[224:227], v161 offset:3072
	ds_read_b128 v[228:231], v161 offset:4096
	ds_read_b128 v[232:235], v161 offset:5120
	ds_read_b128 v[236:239], v161 offset:6144
	ds_read_b128 v[240:243], v161 offset:7168
	global_load_lds_dwordx4 v[196:197], off
	v_lshl_add_u64 v[196:197], s[82:83], 0, v[142:143]
	s_mov_b32 m0, s69
	s_nop 0
	global_load_lds_dwordx4 v[196:197], off
	s_waitcnt vmcnt(8)
	s_waitcnt lgkmcnt(0)
	s_barrier
	s_setprio 1
	s_waitcnt lgkmcnt(0)
	v_mfma_f32_16x16x128_f8f6f4 v[134:137], v[172:179], v[212:219], v[134:137]
	v_mfma_f32_16x16x128_f8f6f4 v[130:133], v[180:187], v[212:219], v[130:133]
	v_mfma_f32_16x16x128_f8f6f4 v[118:121], v[172:179], v[220:227], v[118:121]
	v_mfma_f32_16x16x128_f8f6f4 v[114:117], v[180:187], v[220:227], v[114:117]
	v_mfma_f32_16x16x128_f8f6f4 v[102:105], v[172:179], v[228:235], v[102:105]
	v_mfma_f32_16x16x128_f8f6f4 v[98:101], v[180:187], v[228:235], v[98:101]
	v_mfma_f32_16x16x128_f8f6f4 v[78:81], v[172:179], v[236:243], v[78:81]
	v_mfma_f32_16x16x128_f8f6f4 v[74:77], v[180:187], v[236:243], v[74:77]
	s_setprio 0
	s_setprio 1
	v_mfma_f32_16x16x128_f8f6f4 v[126:129], v[188:195], v[212:219], v[126:129]
	v_mfma_f32_16x16x128_f8f6f4 v[122:125], v[204:211], v[212:219], v[122:125]
	v_mfma_f32_16x16x128_f8f6f4 v[110:113], v[188:195], v[220:227], v[110:113]
	v_mfma_f32_16x16x128_f8f6f4 v[106:109], v[204:211], v[220:227], v[106:109]
	v_mfma_f32_16x16x128_f8f6f4 v[94:97], v[188:195], v[228:235], v[94:97]
	v_mfma_f32_16x16x128_f8f6f4 v[90:93], v[204:211], v[228:235], v[90:93]
	v_mfma_f32_16x16x128_f8f6f4 v[62:65], v[188:195], v[236:243], v[62:65]
	v_mfma_f32_16x16x128_f8f6f4 v[58:61], v[204:211], v[236:243], v[58:61]
	s_setprio 0
	s_barrier
	s_mov_b32 m0, s80
	v_lshl_add_u64 v[196:197], v[150:151], 0, s[34:35]
	s_add_u32 s82, s66, 0x8300
	ds_read_b128 v[212:215], v161 offset:16384
	ds_read_b128 v[216:219], v161 offset:17408
	ds_read_b128 v[220:223], v161 offset:18432
	ds_read_b128 v[224:227], v161 offset:19456
	ds_read_b128 v[228:231], v161 offset:20480
	ds_read_b128 v[232:235], v161 offset:21504
	ds_read_b128 v[236:239], v161 offset:22528
	ds_read_b128 v[240:243], v161 offset:23552
	global_load_lds_dwordx4 v[196:197], off
	v_lshl_add_u64 v[196:197], v[152:153], 0, s[34:35]
	s_mov_b32 m0, s76
	s_addc_u32 s83, s67, 0
	global_load_lds_dwordx4 v[196:197], off
	v_lshl_add_u64 v[196:197], s[82:83], 0, v[140:141]
	s_mov_b32 m0, s77
	s_nop 0
	global_load_lds_dwordx4 v[196:197], off
	v_lshl_add_u64 v[196:197], s[82:83], 0, v[144:145]
	s_mov_b32 m0, s78
	s_nop 0
	global_load_lds_dwordx4 v[196:197], off
	v_lshl_add_u64 v[196:197], v[154:155], 0, s[34:35]
	s_mov_b32 m0, s51
	s_nop 0
	global_load_lds_dwordx4 v[196:197], off
	v_lshl_add_u64 v[196:197], v[156:157], 0, s[34:35]
	s_mov_b32 m0, s57
	s_nop 0
	global_load_lds_dwordx4 v[196:197], off
	s_waitcnt vmcnt(8)
	s_waitcnt lgkmcnt(0)
	s_barrier
	s_setprio 1
	s_waitcnt lgkmcnt(0)
	v_mfma_f32_16x16x128_f8f6f4 v[86:89], v[172:179], v[212:219], v[86:89]
	v_mfma_f32_16x16x128_f8f6f4 v[82:85], v[180:187], v[212:219], v[82:85]
	v_mfma_f32_16x16x128_f8f6f4 v[54:57], v[172:179], v[220:227], v[54:57]
	v_mfma_f32_16x16x128_f8f6f4 v[50:53], v[180:187], v[220:227], v[50:53]
	v_mfma_f32_16x16x128_f8f6f4 v[38:41], v[172:179], v[228:235], v[38:41]
	v_mfma_f32_16x16x128_f8f6f4 v[34:37], v[180:187], v[228:235], v[34:37]
	v_mfma_f32_16x16x128_f8f6f4 v[22:25], v[172:179], v[236:243], v[22:25]
	v_mfma_f32_16x16x128_f8f6f4 v[18:21], v[180:187], v[236:243], v[18:21]
	s_setprio 0
	s_setprio 1
	v_mfma_f32_16x16x128_f8f6f4 v[70:73], v[188:195], v[212:219], v[70:73]
	v_mfma_f32_16x16x128_f8f6f4 v[66:69], v[204:211], v[212:219], v[66:69]
	v_mfma_f32_16x16x128_f8f6f4 v[46:49], v[188:195], v[220:227], v[46:49]
	v_mfma_f32_16x16x128_f8f6f4 v[42:45], v[204:211], v[220:227], v[42:45]
	v_mfma_f32_16x16x128_f8f6f4 v[30:33], v[188:195], v[228:235], v[30:33]
	v_mfma_f32_16x16x128_f8f6f4 v[26:29], v[204:211], v[228:235], v[26:29]
	v_mfma_f32_16x16x128_f8f6f4 v[14:17], v[188:195], v[236:243], v[14:17]
	v_mfma_f32_16x16x128_f8f6f4 v[10:13], v[204:211], v[236:243], v[10:13]
	s_setprio 0
	s_barrier
	ds_read_b128 v[172:175], v158
	ds_read_b128 v[176:179], v158 offset:1024
	ds_read_b128 v[180:183], v158 offset:2048
	ds_read_b128 v[184:187], v158 offset:3072
	ds_read_b128 v[188:191], v159
	ds_read_b128 v[192:195], v159 offset:1024
	ds_read_b128 v[204:207], v159 offset:2048
	ds_read_b128 v[208:211], v159 offset:3072
	s_add_u32 s82, s64, 0x20300
	s_addc_u32 s83, s65, 0
	s_mov_b32 m0, s58
	v_lshl_add_u64 v[196:197], s[82:83], 0, v[138:139]
	ds_read_b128 v[212:215], v161 offset:32768
	ds_read_b128 v[216:219], v161 offset:33792
	ds_read_b128 v[220:223], v161 offset:34816
	ds_read_b128 v[224:227], v161 offset:35840
	ds_read_b128 v[228:231], v161 offset:36864
	ds_read_b128 v[232:235], v161 offset:37888
	ds_read_b128 v[236:239], v161 offset:38912
	ds_read_b128 v[240:243], v161 offset:39936
	global_load_lds_dwordx4 v[196:197], off
	v_lshl_add_u64 v[196:197], s[82:83], 0, v[142:143]
	s_mov_b32 m0, s59
	s_nop 0
	global_load_lds_dwordx4 v[196:197], off
	s_waitcnt vmcnt(8)
	s_waitcnt lgkmcnt(0)
	s_barrier
	s_setprio 1
	s_waitcnt lgkmcnt(0)
	v_mfma_f32_16x16x128_f8f6f4 v[134:137], v[172:179], v[212:219], v[134:137]
	v_mfma_f32_16x16x128_f8f6f4 v[130:133], v[180:187], v[212:219], v[130:133]
	v_mfma_f32_16x16x128_f8f6f4 v[118:121], v[172:179], v[220:227], v[118:121]
	v_mfma_f32_16x16x128_f8f6f4 v[114:117], v[180:187], v[220:227], v[114:117]
	v_mfma_f32_16x16x128_f8f6f4 v[102:105], v[172:179], v[228:235], v[102:105]
	v_mfma_f32_16x16x128_f8f6f4 v[98:101], v[180:187], v[228:235], v[98:101]
	v_mfma_f32_16x16x128_f8f6f4 v[78:81], v[172:179], v[236:243], v[78:81]
	v_mfma_f32_16x16x128_f8f6f4 v[74:77], v[180:187], v[236:243], v[74:77]
	s_setprio 0
	s_setprio 1
	v_mfma_f32_16x16x128_f8f6f4 v[126:129], v[188:195], v[212:219], v[126:129]
	v_mfma_f32_16x16x128_f8f6f4 v[122:125], v[204:211], v[212:219], v[122:125]
	v_mfma_f32_16x16x128_f8f6f4 v[110:113], v[188:195], v[220:227], v[110:113]
	v_mfma_f32_16x16x128_f8f6f4 v[106:109], v[204:211], v[220:227], v[106:109]
	v_mfma_f32_16x16x128_f8f6f4 v[94:97], v[188:195], v[228:235], v[94:97]
	v_mfma_f32_16x16x128_f8f6f4 v[90:93], v[204:211], v[228:235], v[90:93]
	v_mfma_f32_16x16x128_f8f6f4 v[62:65], v[188:195], v[236:243], v[62:65]
	v_mfma_f32_16x16x128_f8f6f4 v[58:61], v[204:211], v[236:243], v[58:61]
	s_setprio 0
	s_barrier
	s_mov_b32 m0, s79
	v_lshl_add_u64 v[150:151], v[150:151], 0, s[36:37]
	s_add_u32 s66, s66, 0x8380
	ds_read_b128 v[212:215], v161 offset:49152
	ds_read_b128 v[216:219], v161 offset:50176
	ds_read_b128 v[220:223], v161 offset:51200
	ds_read_b128 v[224:227], v161 offset:52224
	ds_read_b128 v[228:231], v161 offset:53248
	ds_read_b128 v[232:235], v161 offset:54272
	ds_read_b128 v[236:239], v161 offset:55296
	ds_read_b128 v[240:243], v161 offset:56320
	global_load_lds_dwordx4 v[150:151], off
	v_lshl_add_u64 v[150:151], v[152:153], 0, s[36:37]
	s_mov_b32 m0, s41
	s_addc_u32 s67, s67, 0
	global_load_lds_dwordx4 v[150:151], off
	v_lshl_add_u64 v[150:151], s[66:67], 0, v[140:141]
	s_mov_b32 m0, s43
	s_nop 0
	global_load_lds_dwordx4 v[150:151], off
	v_lshl_add_u64 v[150:151], s[66:67], 0, v[144:145]
	s_mov_b32 m0, s68
	s_nop 0
	global_load_lds_dwordx4 v[150:151], off
	v_lshl_add_u64 v[150:151], v[154:155], 0, s[36:37]
	s_mov_b32 m0, s60
	s_nop 0
	global_load_lds_dwordx4 v[150:151], off
	v_lshl_add_u64 v[150:151], v[156:157], 0, s[36:37]
	s_mov_b32 m0, s61
	s_nop 0
	global_load_lds_dwordx4 v[150:151], off
	s_waitcnt vmcnt(8)
	s_waitcnt lgkmcnt(0)
	s_barrier
	s_setprio 1
	s_waitcnt lgkmcnt(0)
	v_mfma_f32_16x16x128_f8f6f4 v[86:89], v[172:179], v[212:219], v[86:89]
	v_mfma_f32_16x16x128_f8f6f4 v[82:85], v[180:187], v[212:219], v[82:85]
	v_mfma_f32_16x16x128_f8f6f4 v[54:57], v[172:179], v[220:227], v[54:57]
	v_mfma_f32_16x16x128_f8f6f4 v[50:53], v[180:187], v[220:227], v[50:53]
	v_mfma_f32_16x16x128_f8f6f4 v[38:41], v[172:179], v[228:235], v[38:41]
	v_mfma_f32_16x16x128_f8f6f4 v[34:37], v[180:187], v[228:235], v[34:37]
	v_mfma_f32_16x16x128_f8f6f4 v[22:25], v[172:179], v[236:243], v[22:25]
	v_mfma_f32_16x16x128_f8f6f4 v[18:21], v[180:187], v[236:243], v[18:21]
	s_setprio 0
	s_setprio 1
	v_mfma_f32_16x16x128_f8f6f4 v[70:73], v[188:195], v[212:219], v[70:73]
	v_mfma_f32_16x16x128_f8f6f4 v[66:69], v[204:211], v[212:219], v[66:69]
	v_mfma_f32_16x16x128_f8f6f4 v[46:49], v[188:195], v[220:227], v[46:49]
	v_mfma_f32_16x16x128_f8f6f4 v[42:45], v[204:211], v[220:227], v[42:45]
	v_mfma_f32_16x16x128_f8f6f4 v[30:33], v[188:195], v[228:235], v[30:33]
	v_mfma_f32_16x16x128_f8f6f4 v[26:29], v[204:211], v[228:235], v[26:29]
	v_mfma_f32_16x16x128_f8f6f4 v[14:17], v[188:195], v[236:243], v[14:17]
	v_mfma_f32_16x16x128_f8f6f4 v[10:13], v[204:211], v[236:243], v[10:13]
	s_setprio 0
	s_barrier
	ds_read_b128 v[150:153], v162
	ds_read_b128 v[154:157], v162 offset:1024
	ds_read_b128 v[172:175], v162 offset:2048
	ds_read_b128 v[176:179], v162 offset:3072
	ds_read_b128 v[180:183], v163
	ds_read_b128 v[184:187], v163 offset:1024
	ds_read_b128 v[188:191], v163 offset:2048
	ds_read_b128 v[192:195], v163 offset:3072
	s_add_u32 s64, s64, 0x20380
	s_addc_u32 s65, s65, 0
	s_mov_b32 m0, s63
	v_lshl_add_u64 v[196:197], s[64:65], 0, v[138:139]
	ds_read_b128 v[204:207], v161
	ds_read_b128 v[208:211], v161 offset:1024
	ds_read_b128 v[212:215], v161 offset:2048
	ds_read_b128 v[216:219], v161 offset:3072
	ds_read_b128 v[220:223], v161 offset:4096
	ds_read_b128 v[224:227], v161 offset:5120
	ds_read_b128 v[228:231], v161 offset:6144
	ds_read_b128 v[232:235], v161 offset:7168
	global_load_lds_dwordx4 v[196:197], off
	v_lshl_add_u64 v[196:197], s[64:65], 0, v[142:143]
	s_mov_b32 m0, s69
	s_nop 0
	global_load_lds_dwordx4 v[196:197], off
	s_waitcnt vmcnt(8)
	s_waitcnt lgkmcnt(0)
	s_barrier
	s_setprio 1
	s_waitcnt lgkmcnt(0)
	v_mfma_f32_16x16x128_f8f6f4 v[134:137], v[150:157], v[204:211], v[134:137]
	v_mfma_f32_16x16x128_f8f6f4 v[130:133], v[172:179], v[204:211], v[130:133]
	v_mfma_f32_16x16x128_f8f6f4 v[118:121], v[150:157], v[212:219], v[118:121]
	v_mfma_f32_16x16x128_f8f6f4 v[114:117], v[172:179], v[212:219], v[114:117]
	v_mfma_f32_16x16x128_f8f6f4 v[102:105], v[150:157], v[220:227], v[102:105]
	v_mfma_f32_16x16x128_f8f6f4 v[98:101], v[172:179], v[220:227], v[98:101]
	v_mfma_f32_16x16x128_f8f6f4 v[78:81], v[150:157], v[228:235], v[78:81]
	v_mfma_f32_16x16x128_f8f6f4 v[74:77], v[172:179], v[228:235], v[74:77]
	s_setprio 0
	s_setprio 1
	v_mfma_f32_16x16x128_f8f6f4 v[126:129], v[180:187], v[204:211], v[126:129]
	v_mfma_f32_16x16x128_f8f6f4 v[122:125], v[188:195], v[204:211], v[122:125]
	v_mfma_f32_16x16x128_f8f6f4 v[110:113], v[180:187], v[212:219], v[110:113]
	v_mfma_f32_16x16x128_f8f6f4 v[106:109], v[188:195], v[212:219], v[106:109]
	v_mfma_f32_16x16x128_f8f6f4 v[94:97], v[180:187], v[220:227], v[94:97]
	v_mfma_f32_16x16x128_f8f6f4 v[90:93], v[188:195], v[220:227], v[90:93]
	v_mfma_f32_16x16x128_f8f6f4 v[62:65], v[180:187], v[228:235], v[62:65]
	v_mfma_f32_16x16x128_f8f6f4 v[58:61], v[188:195], v[228:235], v[58:61]
	s_setprio 0
	s_barrier
	s_mov_b32 m0, s80
	v_lshl_add_u64 v[196:197], s[10:11], 0, v[140:141]
	s_add_u32 s64, s10, 0x8000
	ds_read_b128 v[204:207], v161 offset:16384
	ds_read_b128 v[208:211], v161 offset:17408
	ds_read_b128 v[212:215], v161 offset:18432
	ds_read_b128 v[216:219], v161 offset:19456
	ds_read_b128 v[220:223], v161 offset:20480
	ds_read_b128 v[224:227], v161 offset:21504
	ds_read_b128 v[228:231], v161 offset:22528
	ds_read_b128 v[232:235], v161 offset:23552
	global_load_lds_dwordx4 v[196:197], off
	v_lshl_add_u64 v[198:199], s[10:11], 0, v[144:145]
	s_mov_b32 m0, s76
	s_addc_u32 s65, s11, 0
	global_load_lds_dwordx4 v[198:199], off
	v_lshl_add_u64 v[200:201], s[64:65], 0, v[140:141]
	s_mov_b32 m0, s77
	v_lshl_add_u64 v[236:237], s[70:71], 0, v[142:143]
	global_load_lds_dwordx4 v[200:201], off
	v_lshl_add_u64 v[200:201], s[64:65], 0, v[144:145]
	s_mov_b32 m0, s78
	s_nop 0
	global_load_lds_dwordx4 v[200:201], off
	v_lshl_add_u64 v[200:201], s[70:71], 0, v[138:139]
	s_mov_b32 m0, s51
	s_nop 0
	global_load_lds_dwordx4 v[200:201], off
	s_mov_b32 m0, s57
	s_nop 0
	global_load_lds_dwordx4 v[236:237], off
	s_waitcnt vmcnt(8)
	s_waitcnt lgkmcnt(0)
	s_barrier
	s_setprio 1
	s_waitcnt lgkmcnt(0)
	v_mfma_f32_16x16x128_f8f6f4 v[86:89], v[150:157], v[204:211], v[86:89]
	v_mfma_f32_16x16x128_f8f6f4 v[82:85], v[172:179], v[204:211], v[82:85]
	v_mfma_f32_16x16x128_f8f6f4 v[54:57], v[150:157], v[212:219], v[54:57]
	v_mfma_f32_16x16x128_f8f6f4 v[50:53], v[172:179], v[212:219], v[50:53]
	v_mfma_f32_16x16x128_f8f6f4 v[38:41], v[150:157], v[220:227], v[38:41]
	v_mfma_f32_16x16x128_f8f6f4 v[34:37], v[172:179], v[220:227], v[34:37]
	v_mfma_f32_16x16x128_f8f6f4 v[22:25], v[150:157], v[228:235], v[22:25]
	v_mfma_f32_16x16x128_f8f6f4 v[18:21], v[172:179], v[228:235], v[18:21]
	s_setprio 0
	s_setprio 1
	v_mfma_f32_16x16x128_f8f6f4 v[70:73], v[180:187], v[204:211], v[70:73]
	v_mfma_f32_16x16x128_f8f6f4 v[66:69], v[188:195], v[204:211], v[66:69]
	v_mfma_f32_16x16x128_f8f6f4 v[46:49], v[180:187], v[212:219], v[46:49]
	v_mfma_f32_16x16x128_f8f6f4 v[42:45], v[188:195], v[212:219], v[42:45]
	v_mfma_f32_16x16x128_f8f6f4 v[30:33], v[180:187], v[220:227], v[30:33]
	v_mfma_f32_16x16x128_f8f6f4 v[26:29], v[188:195], v[220:227], v[26:29]
	v_mfma_f32_16x16x128_f8f6f4 v[14:17], v[180:187], v[228:235], v[14:17]
	v_mfma_f32_16x16x128_f8f6f4 v[10:13], v[188:195], v[228:235], v[10:13]
	s_setprio 0
	s_barrier
	ds_read_b128 v[150:153], v158
	ds_read_b128 v[154:157], v158 offset:1024
	ds_read_b128 v[172:175], v158 offset:2048
	ds_read_b128 v[176:179], v158 offset:3072
	ds_read_b128 v[180:183], v159
	ds_read_b128 v[184:187], v159 offset:1024
	ds_read_b128 v[188:191], v159 offset:2048
	ds_read_b128 v[192:195], v159 offset:3072
	s_add_u32 s64, s70, 0x20000
	s_addc_u32 s65, s71, 0
	s_mov_b32 m0, s58
	v_lshl_add_u64 v[158:159], s[64:65], 0, v[138:139]
	ds_read_b128 v[204:207], v161 offset:32768
	ds_read_b128 v[208:211], v161 offset:33792
	ds_read_b128 v[212:215], v161 offset:34816
	ds_read_b128 v[216:219], v161 offset:35840
	ds_read_b128 v[220:223], v161 offset:36864
	ds_read_b128 v[224:227], v161 offset:37888
	ds_read_b128 v[228:231], v161 offset:38912
	ds_read_b128 v[232:235], v161 offset:39936
	global_load_lds_dwordx4 v[158:159], off
	v_lshl_add_u64 v[158:159], s[64:65], 0, v[142:143]
	s_mov_b32 m0, s59
	s_nop 0
	global_load_lds_dwordx4 v[158:159], off
	s_waitcnt vmcnt(8)
	s_waitcnt lgkmcnt(0)
	s_barrier
	s_setprio 1
	s_waitcnt lgkmcnt(0)
	v_mfma_f32_16x16x128_f8f6f4 v[134:137], v[150:157], v[204:211], v[134:137]
	v_mfma_f32_16x16x128_f8f6f4 v[130:133], v[172:179], v[204:211], v[130:133]
	v_mfma_f32_16x16x128_f8f6f4 v[118:121], v[150:157], v[212:219], v[118:121]
	v_mfma_f32_16x16x128_f8f6f4 v[114:117], v[172:179], v[212:219], v[114:117]
	v_mfma_f32_16x16x128_f8f6f4 v[102:105], v[150:157], v[220:227], v[102:105]
	v_mfma_f32_16x16x128_f8f6f4 v[98:101], v[172:179], v[220:227], v[98:101]
	v_mfma_f32_16x16x128_f8f6f4 v[78:81], v[150:157], v[228:235], v[78:81]
	v_mfma_f32_16x16x128_f8f6f4 v[74:77], v[172:179], v[228:235], v[74:77]
	s_setprio 0
	s_setprio 1
	v_mfma_f32_16x16x128_f8f6f4 v[126:129], v[180:187], v[204:211], v[126:129]
	v_mfma_f32_16x16x128_f8f6f4 v[122:125], v[188:195], v[204:211], v[122:125]
	v_mfma_f32_16x16x128_f8f6f4 v[110:113], v[180:187], v[212:219], v[110:113]
	v_mfma_f32_16x16x128_f8f6f4 v[106:109], v[188:195], v[212:219], v[106:109]
	v_mfma_f32_16x16x128_f8f6f4 v[94:97], v[180:187], v[220:227], v[94:97]
	v_mfma_f32_16x16x128_f8f6f4 v[90:93], v[188:195], v[220:227], v[90:93]
	v_mfma_f32_16x16x128_f8f6f4 v[62:65], v[180:187], v[228:235], v[62:65]
	v_mfma_f32_16x16x128_f8f6f4 v[58:61], v[188:195], v[228:235], v[58:61]
	s_setprio 0
	s_barrier
	s_mov_b32 m0, s79
	v_lshl_add_u64 v[158:159], v[196:197], 0, s[18:19]
	s_add_u32 s10, s10, 0x8080
	ds_read_b128 v[204:207], v161 offset:49152
	ds_read_b128 v[208:211], v161 offset:50176
	ds_read_b128 v[212:215], v161 offset:51200
	ds_read_b128 v[216:219], v161 offset:52224
	ds_read_b128 v[220:223], v161 offset:53248
	ds_read_b128 v[224:227], v161 offset:54272
	ds_read_b128 v[228:231], v161 offset:55296
	ds_read_b128 v[232:235], v161 offset:56320
	global_load_lds_dwordx4 v[158:159], off
	v_lshl_add_u64 v[158:159], v[198:199], 0, s[18:19]
	s_mov_b32 m0, s41
	s_addc_u32 s11, s11, 0
	global_load_lds_dwordx4 v[158:159], off
	v_lshl_add_u64 v[158:159], s[10:11], 0, v[140:141]
	s_mov_b32 m0, s43
	s_nop 0
	global_load_lds_dwordx4 v[158:159], off
	v_lshl_add_u64 v[158:159], s[10:11], 0, v[144:145]
	s_mov_b32 m0, s68
	s_nop 0
	global_load_lds_dwordx4 v[158:159], off
	v_lshl_add_u64 v[158:159], v[200:201], 0, s[18:19]
	s_mov_b32 m0, s60
	s_nop 0
	global_load_lds_dwordx4 v[158:159], off
	v_lshl_add_u64 v[158:159], v[236:237], 0, s[18:19]
	s_mov_b32 m0, s61
	s_nop 0
	global_load_lds_dwordx4 v[158:159], off
	s_waitcnt vmcnt(8)
	s_waitcnt lgkmcnt(0)
	s_barrier
	s_setprio 1
	s_waitcnt lgkmcnt(0)
	v_mfma_f32_16x16x128_f8f6f4 v[86:89], v[150:157], v[204:211], v[86:89]
	v_mfma_f32_16x16x128_f8f6f4 v[82:85], v[172:179], v[204:211], v[82:85]
	v_mfma_f32_16x16x128_f8f6f4 v[54:57], v[150:157], v[212:219], v[54:57]
	v_mfma_f32_16x16x128_f8f6f4 v[50:53], v[172:179], v[212:219], v[50:53]
	v_mfma_f32_16x16x128_f8f6f4 v[38:41], v[150:157], v[220:227], v[38:41]
	v_mfma_f32_16x16x128_f8f6f4 v[34:37], v[172:179], v[220:227], v[34:37]
	v_mfma_f32_16x16x128_f8f6f4 v[22:25], v[150:157], v[228:235], v[22:25]
	v_mfma_f32_16x16x128_f8f6f4 v[18:21], v[172:179], v[228:235], v[18:21]
	s_setprio 0
	s_setprio 1
	v_mfma_f32_16x16x128_f8f6f4 v[70:73], v[180:187], v[204:211], v[70:73]
	v_mfma_f32_16x16x128_f8f6f4 v[66:69], v[188:195], v[204:211], v[66:69]
	v_mfma_f32_16x16x128_f8f6f4 v[46:49], v[180:187], v[212:219], v[46:49]
	v_mfma_f32_16x16x128_f8f6f4 v[42:45], v[188:195], v[212:219], v[42:45]
	v_mfma_f32_16x16x128_f8f6f4 v[30:33], v[180:187], v[220:227], v[30:33]
	v_mfma_f32_16x16x128_f8f6f4 v[26:29], v[188:195], v[220:227], v[26:29]
	v_mfma_f32_16x16x128_f8f6f4 v[14:17], v[180:187], v[228:235], v[14:17]
	v_mfma_f32_16x16x128_f8f6f4 v[10:13], v[188:195], v[228:235], v[10:13]
	s_setprio 0
	s_barrier
	v_cndmask_b32_e64 v150, 0, 1, s[8:9]
	v_cmp_ne_u32_e64 s[10:11], 1, v150
	s_andn2_b64 vcc, exec, s[8:9]
	s_cbranch_vccnz .LBB0_3427
	s_add_u32 s8, s46, 0x20080
	s_addc_u32 s9, s47, 0
	s_mov_b32 m0, s63
	v_lshl_add_u64 v[150:151], s[8:9], 0, v[138:139]
	v_lshl_add_u64 v[152:153], s[8:9], 0, v[142:143]
	global_load_lds_dwordx4 v[150:151], off
	s_mov_b32 m0, s69
	s_nop 0
	global_load_lds_dwordx4 v[152:153], off
